# speedup vs baseline: 1.0198x; 1.0044x over previous
_Z12k1_colsum_q8PKfPjPfS2_:
	s_load_dwordx8 s[4:11], s[0:1], 0x0
	v_and_b32_e32 v1, 63, v0
	v_lshrrev_b32_e32 v41, 6, v0
	s_mul_i32 s12, s2, 0xc35
	s_lshr_b32 s12, s12, 4
	v_readfirstlane_b32 s14, v41
	s_add_i32 s13, s2, 1
	s_mul_i32 s13, s13, 0xc35
	s_lshr_b32 s13, s13, 4
	s_sub_u32 s13, s13, s12
	s_sub_u32 s15, s13, 0xc0
	s_cmp_lt_u32 s14, s15
	s_cselect_b32 s29, 1, 0
	v_lshlrev_b32_e32 v34, 4, v1
	v_min_u32_e32 v35, 57, v1
	v_lshlrev_b32_e32 v35, 4, v35
	v_cmp_gt_u32_e64 s[18:19], 58, v1
	s_lshl_b32 s35, s14, 13
	s_add_u32 s36, s35, 0x1000
	v_add_u32_e32 v38, s35, v34
	v_lshrrev_b32_e32 v41, 5, v1
	v_mov_b32_e32 v42, 0xc35000
	v_mul_lo_u32 v39, v41, v42
	v_and_b32_e32 v42, 31, v1
	v_lshl_add_u32 v39, v42, 2, v39
	v_mov_b32_e32 v2, 0
	v_mov_b32_e32 v3, 0
	v_mov_b32_e32 v4, 0
	v_mov_b32_e32 v5, 0
	v_mov_b32_e32 v6, 0
	v_mov_b32_e32 v7, 0
	v_mov_b32_e32 v8, 0
	v_mov_b32_e32 v9, 0
	v_mov_b32_e32 v10, 0
	v_mov_b32_e32 v11, 0
	v_mov_b32_e32 v12, 0
	v_mov_b32_e32 v13, 0
	v_mov_b32_e32 v14, 0
	v_mov_b32_e32 v15, 0
	v_mov_b32_e32 v16, 0
	v_mov_b32_e32 v17, 0
	v_mov_b32_e32 v40, 0
	v_mov_b32_e32 v47, 0x42fe0000
	s_mov_b32 s32, 0x42fe0000
	s_mov_b32 s33, 0xc0c0400
	s_mov_b32 s34, 0x4000c0c
	s_add_u32 s15, s12, s14
	s_mul_i32 s37, s15, 0xfa0
	s_lshl_b32 s15, s15, 7
	s_waitcnt lgkmcnt(0)
	s_add_u32 s16, s4, s37
	s_addc_u32 s17, s5, 0
	s_add_u32 s40, s6, s15
	s_addc_u32 s41, s7, 0
	s_add_u32 s20, s40, 0
	s_addc_u32 s21, s41, 0
	s_add_u32 s22, s20, 0x186a000
	s_addc_u32 s23, s21, 0
	s_add_u32 s24, s22, 0x186a000
	s_addc_u32 s25, s23, 0
	s_add_u32 s26, s24, 0x186a000
	s_addc_u32 s27, s25, 0
	s_mov_b32 m0, s35
	s_nop 0
	global_load_lds_dwordx4 v34, s[16:17] nt
	global_load_lds_dwordx4 v34, s[16:17] offset:1024 nt
	global_load_lds_dwordx4 v34, s[16:17] offset:2048 nt
	global_load_lds_dwordx4 v35, s[16:17] offset:3072 nt
	s_add_u32 s16, s16, 0x7d00
	s_addc_u32 s17, s17, 0
	s_waitcnt vmcnt(0)
	ds_read_b128 v[18:21], v38 offset:0
	ds_read_b128 v[22:25], v38 offset:1024
	ds_read_b128 v[26:29], v38 offset:2048
	ds_read_b128 v[30:33], v38 offset:3072
	s_waitcnt lgkmcnt(0)
	s_barrier
	s_mov_b32 m0, s36
	s_nop 0
	global_load_lds_dwordx4 v34, s[16:17] nt
	global_load_lds_dwordx4 v34, s[16:17] offset:1024 nt
	global_load_lds_dwordx4 v34, s[16:17] offset:2048 nt
	global_load_lds_dwordx4 v35, s[16:17] offset:3072 nt
	s_add_u32 s16, s16, 0x7d00
	s_addc_u32 s17, s17, 0
	v_cndmask_b32_e64 v30, 0, v30, s[18:19]
	v_cndmask_b32_e64 v31, 0, v31, s[18:19]
	v_cndmask_b32_e64 v32, 0, v32, s[18:19]
	v_cndmask_b32_e64 v33, 0, v33, s[18:19]
	v_max3_f32 v41, |v18|, |v19|, |v20|
	v_max3_f32 v42, |v21|, |v22|, |v23|
	v_max3_f32 v43, |v24|, |v25|, |v26|
	v_max3_f32 v44, |v27|, |v28|, |v29|
	v_max3_f32 v48, |v30|, |v31|, |v32|
	v_max3_f32 v41, v41, v42, |v33|
	v_max3_f32 v43, v43, v44, v48
	v_max_f32_e32 v41, v41, v43
	v_pk_add_f32 v[2:3], v[2:3], v[18:19]
	v_pk_add_f32 v[4:5], v[4:5], v[20:21]
	v_max_f32_dpp v41, v41, v41 quad_perm:[1,0,3,2] row_mask:0xf bank_mask:0xf
	v_pk_add_f32 v[6:7], v[6:7], v[22:23]
	v_pk_add_f32 v[8:9], v[8:9], v[24:25]
	v_max_f32_dpp v41, v41, v41 quad_perm:[2,3,0,1] row_mask:0xf bank_mask:0xf
	v_pk_add_f32 v[10:11], v[10:11], v[26:27]
	v_pk_add_f32 v[12:13], v[12:13], v[28:29]
	v_max_f32_dpp v41, v41, v41 row_half_mirror row_mask:0xf bank_mask:0xf
	v_pk_add_f32 v[14:15], v[14:15], v[30:31]
	v_pk_add_f32 v[16:17], v[16:17], v[32:33]
	v_max_f32_dpp v41, v41, v41 row_mirror row_mask:0xf bank_mask:0xf
	s_nop 1
	v_max_f32_dpp v41, v41, v41 row_bcast:15 row_mask:0xa bank_mask:0xf
	s_nop 1
	v_max_f32_dpp v41, v41, v41 row_bcast:31 row_mask:0xc bank_mask:0xf
	s_nop 1
	v_readlane_b32 s28, v41, 63
	s_nop 1
	v_div_scale_f32 v48, s[30:31], s28, s28, v47
	v_rcp_f32_e32 v49, v48
	s_nop 0
	v_fma_f32 v50, -v48, v49, 1.0
	v_fmac_f32_e32 v49, v50, v49
	v_mov_b32_e32 v50, s28
	v_div_scale_f32 v50, vcc, s32, v50, s32
	v_mul_f32_e32 v51, v50, v49
	v_fma_f32 v52, -v48, v51, v50
	v_fmac_f32_e32 v51, v52, v49
	v_fma_f32 v48, -v48, v51, v50
	v_div_fmas_f32 v48, v48, v49, v51
	v_div_fixup_f32 v48, v48, s28, v47
	v_cmp_gt_f32_e64 vcc, s28, 0
	v_writelane_b32 v40, s28, 0
	s_nop 0
	v_cndmask_b32_e32 v48, 0, v48, vcc
	v_fmaak_f32 v49, v18, v48, 0x4b400000
	v_fmaak_f32 v50, v19, v48, 0x4b400000
	v_fmaak_f32 v51, v20, v48, 0x4b400000
	v_fmaak_f32 v52, v21, v48, 0x4b400000
	v_perm_b32 v49, v50, v49, s33
	v_perm_b32 v51, v52, v51, s34
	v_or_b32_e32 v56, v49, v51
	v_fmaak_f32 v41, v22, v48, 0x4b400000
	v_fmaak_f32 v42, v23, v48, 0x4b400000
	v_fmaak_f32 v43, v24, v48, 0x4b400000
	v_fmaak_f32 v44, v25, v48, 0x4b400000
	v_perm_b32 v41, v42, v41, s33
	v_perm_b32 v43, v44, v43, s34
	v_or_b32_e32 v57, v41, v43
	v_fmaak_f32 v49, v26, v48, 0x4b400000
	v_fmaak_f32 v50, v27, v48, 0x4b400000
	v_fmaak_f32 v51, v28, v48, 0x4b400000
	v_fmaak_f32 v52, v29, v48, 0x4b400000
	v_perm_b32 v49, v50, v49, s33
	v_perm_b32 v51, v52, v51, s34
	v_or_b32_e32 v58, v49, v51
	v_fmaak_f32 v41, v30, v48, 0x4b400000
	v_fmaak_f32 v42, v31, v48, 0x4b400000
	v_fmaak_f32 v43, v32, v48, 0x4b400000
	v_fmaak_f32 v44, v33, v48, 0x4b400000
	v_perm_b32 v41, v42, v41, s33
	v_perm_b32 v43, v44, v43, s34
	v_or_b32_e32 v59, v41, v43
	s_waitcnt vmcnt(0)
	ds_read_b128 v[18:21], v38 offset:4096
	ds_read_b128 v[22:25], v38 offset:5120
	ds_read_b128 v[26:29], v38 offset:6144
	ds_read_b128 v[30:33], v38 offset:7168
	s_waitcnt lgkmcnt(0)
	s_barrier
	s_mov_b32 m0, s35
	s_nop 0
	global_load_lds_dwordx4 v34, s[16:17] nt
	global_load_lds_dwordx4 v34, s[16:17] offset:1024 nt
	global_load_lds_dwordx4 v34, s[16:17] offset:2048 nt
	global_load_lds_dwordx4 v35, s[16:17] offset:3072 nt
	s_add_u32 s16, s16, 0x7d00
	s_addc_u32 s17, s17, 0
	v_cndmask_b32_e64 v30, 0, v30, s[18:19]
	v_cndmask_b32_e64 v31, 0, v31, s[18:19]
	v_cndmask_b32_e64 v32, 0, v32, s[18:19]
	v_cndmask_b32_e64 v33, 0, v33, s[18:19]
	v_max3_f32 v41, |v18|, |v19|, |v20|
	v_max3_f32 v42, |v21|, |v22|, |v23|
	v_max3_f32 v43, |v24|, |v25|, |v26|
	v_max3_f32 v44, |v27|, |v28|, |v29|
	v_max3_f32 v48, |v30|, |v31|, |v32|
	v_max3_f32 v41, v41, v42, |v33|
	v_max3_f32 v43, v43, v44, v48
	v_max_f32_e32 v41, v41, v43
	v_pk_add_f32 v[2:3], v[2:3], v[18:19]
	v_pk_add_f32 v[4:5], v[4:5], v[20:21]
	v_max_f32_dpp v41, v41, v41 quad_perm:[1,0,3,2] row_mask:0xf bank_mask:0xf
	v_pk_add_f32 v[6:7], v[6:7], v[22:23]
	v_pk_add_f32 v[8:9], v[8:9], v[24:25]
	v_max_f32_dpp v41, v41, v41 quad_perm:[2,3,0,1] row_mask:0xf bank_mask:0xf
	v_pk_add_f32 v[10:11], v[10:11], v[26:27]
	v_pk_add_f32 v[12:13], v[12:13], v[28:29]
	v_max_f32_dpp v41, v41, v41 row_half_mirror row_mask:0xf bank_mask:0xf
	v_pk_add_f32 v[14:15], v[14:15], v[30:31]
	v_pk_add_f32 v[16:17], v[16:17], v[32:33]
	v_max_f32_dpp v41, v41, v41 row_mirror row_mask:0xf bank_mask:0xf
	s_nop 1
	v_max_f32_dpp v41, v41, v41 row_bcast:15 row_mask:0xa bank_mask:0xf
	s_nop 1
	v_max_f32_dpp v41, v41, v41 row_bcast:31 row_mask:0xc bank_mask:0xf
	s_nop 1
	v_readlane_b32 s28, v41, 63
	s_nop 1
	v_div_scale_f32 v48, s[30:31], s28, s28, v47
	v_rcp_f32_e32 v49, v48
	s_nop 0
	v_fma_f32 v50, -v48, v49, 1.0
	v_fmac_f32_e32 v49, v50, v49
	v_mov_b32_e32 v50, s28
	v_div_scale_f32 v50, vcc, s32, v50, s32
	v_mul_f32_e32 v51, v50, v49
	v_fma_f32 v52, -v48, v51, v50
	v_fmac_f32_e32 v51, v52, v49
	v_fma_f32 v48, -v48, v51, v50
	v_div_fmas_f32 v48, v48, v49, v51
	v_div_fixup_f32 v48, v48, s28, v47
	v_cmp_gt_f32_e64 vcc, s28, 0
	v_writelane_b32 v40, s28, 1
	s_nop 0
	v_cndmask_b32_e32 v48, 0, v48, vcc
	v_fmaak_f32 v49, v18, v48, 0x4b400000
	v_fmaak_f32 v50, v19, v48, 0x4b400000
	v_fmaak_f32 v51, v20, v48, 0x4b400000
	v_fmaak_f32 v52, v21, v48, 0x4b400000
	v_perm_b32 v49, v50, v49, s33
	v_perm_b32 v51, v52, v51, s34
	v_or_b32_e32 v60, v49, v51
	v_fmaak_f32 v41, v22, v48, 0x4b400000
	v_fmaak_f32 v42, v23, v48, 0x4b400000
	v_fmaak_f32 v43, v24, v48, 0x4b400000
	v_fmaak_f32 v44, v25, v48, 0x4b400000
	v_perm_b32 v41, v42, v41, s33
	v_perm_b32 v43, v44, v43, s34
	v_or_b32_e32 v61, v41, v43
	v_fmaak_f32 v49, v26, v48, 0x4b400000
	v_fmaak_f32 v50, v27, v48, 0x4b400000
	v_fmaak_f32 v51, v28, v48, 0x4b400000
	v_fmaak_f32 v52, v29, v48, 0x4b400000
	v_perm_b32 v49, v50, v49, s33
	v_perm_b32 v51, v52, v51, s34
	v_or_b32_e32 v62, v49, v51
	v_fmaak_f32 v41, v30, v48, 0x4b400000
	v_fmaak_f32 v42, v31, v48, 0x4b400000
	v_fmaak_f32 v43, v32, v48, 0x4b400000
	v_fmaak_f32 v44, v33, v48, 0x4b400000
	v_perm_b32 v41, v42, v41, s33
	v_perm_b32 v43, v44, v43, s34
	v_or_b32_e32 v63, v41, v43
	s_waitcnt vmcnt(0)
	ds_read_b128 v[18:21], v38 offset:0
	ds_read_b128 v[22:25], v38 offset:1024
	ds_read_b128 v[26:29], v38 offset:2048
	ds_read_b128 v[30:33], v38 offset:3072
	s_waitcnt lgkmcnt(0)
	s_barrier
	s_mov_b32 m0, s36
	s_nop 0
	global_load_lds_dwordx4 v34, s[16:17] nt
	global_load_lds_dwordx4 v34, s[16:17] offset:1024 nt
	global_load_lds_dwordx4 v34, s[16:17] offset:2048 nt
	global_load_lds_dwordx4 v35, s[16:17] offset:3072 nt
	s_add_u32 s16, s16, 0x7d00
	s_addc_u32 s17, s17, 0
	v_cndmask_b32_e64 v30, 0, v30, s[18:19]
	v_cndmask_b32_e64 v31, 0, v31, s[18:19]
	v_cndmask_b32_e64 v32, 0, v32, s[18:19]
	v_cndmask_b32_e64 v33, 0, v33, s[18:19]
	v_max3_f32 v41, |v18|, |v19|, |v20|
	v_max3_f32 v42, |v21|, |v22|, |v23|
	v_max3_f32 v43, |v24|, |v25|, |v26|
	v_max3_f32 v44, |v27|, |v28|, |v29|
	v_max3_f32 v48, |v30|, |v31|, |v32|
	v_max3_f32 v41, v41, v42, |v33|
	v_max3_f32 v43, v43, v44, v48
	v_max_f32_e32 v41, v41, v43
	v_pk_add_f32 v[2:3], v[2:3], v[18:19]
	v_pk_add_f32 v[4:5], v[4:5], v[20:21]
	v_max_f32_dpp v41, v41, v41 quad_perm:[1,0,3,2] row_mask:0xf bank_mask:0xf
	v_pk_add_f32 v[6:7], v[6:7], v[22:23]
	v_pk_add_f32 v[8:9], v[8:9], v[24:25]
	v_max_f32_dpp v41, v41, v41 quad_perm:[2,3,0,1] row_mask:0xf bank_mask:0xf
	v_pk_add_f32 v[10:11], v[10:11], v[26:27]
	v_pk_add_f32 v[12:13], v[12:13], v[28:29]
	v_max_f32_dpp v41, v41, v41 row_half_mirror row_mask:0xf bank_mask:0xf
	v_pk_add_f32 v[14:15], v[14:15], v[30:31]
	v_pk_add_f32 v[16:17], v[16:17], v[32:33]
	v_max_f32_dpp v41, v41, v41 row_mirror row_mask:0xf bank_mask:0xf
	s_nop 1
	v_max_f32_dpp v41, v41, v41 row_bcast:15 row_mask:0xa bank_mask:0xf
	s_nop 1
	v_max_f32_dpp v41, v41, v41 row_bcast:31 row_mask:0xc bank_mask:0xf
	s_nop 1
	v_readlane_b32 s28, v41, 63
	s_nop 1
	v_div_scale_f32 v48, s[30:31], s28, s28, v47
	v_rcp_f32_e32 v49, v48
	s_nop 0
	v_fma_f32 v50, -v48, v49, 1.0
	v_fmac_f32_e32 v49, v50, v49
	v_mov_b32_e32 v50, s28
	v_div_scale_f32 v50, vcc, s32, v50, s32
	v_mul_f32_e32 v51, v50, v49
	v_fma_f32 v52, -v48, v51, v50
	v_fmac_f32_e32 v51, v52, v49
	v_fma_f32 v48, -v48, v51, v50
	v_div_fmas_f32 v48, v48, v49, v51
	v_div_fixup_f32 v48, v48, s28, v47
	v_cmp_gt_f32_e64 vcc, s28, 0
	v_writelane_b32 v40, s28, 2
	s_nop 0
	v_cndmask_b32_e32 v48, 0, v48, vcc
	v_fmaak_f32 v49, v18, v48, 0x4b400000
	v_fmaak_f32 v50, v19, v48, 0x4b400000
	v_fmaak_f32 v51, v20, v48, 0x4b400000
	v_fmaak_f32 v52, v21, v48, 0x4b400000
	v_perm_b32 v49, v50, v49, s33
	v_perm_b32 v51, v52, v51, s34
	v_or_b32_e32 v64, v49, v51
	v_fmaak_f32 v41, v22, v48, 0x4b400000
	v_fmaak_f32 v42, v23, v48, 0x4b400000
	v_fmaak_f32 v43, v24, v48, 0x4b400000
	v_fmaak_f32 v44, v25, v48, 0x4b400000
	v_perm_b32 v41, v42, v41, s33
	v_perm_b32 v43, v44, v43, s34
	v_or_b32_e32 v65, v41, v43
	v_fmaak_f32 v49, v26, v48, 0x4b400000
	v_fmaak_f32 v50, v27, v48, 0x4b400000
	v_fmaak_f32 v51, v28, v48, 0x4b400000
	v_fmaak_f32 v52, v29, v48, 0x4b400000
	v_perm_b32 v49, v50, v49, s33
	v_perm_b32 v51, v52, v51, s34
	v_or_b32_e32 v66, v49, v51
	v_fmaak_f32 v41, v30, v48, 0x4b400000
	v_fmaak_f32 v42, v31, v48, 0x4b400000
	v_fmaak_f32 v43, v32, v48, 0x4b400000
	v_fmaak_f32 v44, v33, v48, 0x4b400000
	v_perm_b32 v41, v42, v41, s33
	v_perm_b32 v43, v44, v43, s34
	v_or_b32_e32 v67, v41, v43
	s_waitcnt vmcnt(0)
	ds_read_b128 v[18:21], v38 offset:4096
	ds_read_b128 v[22:25], v38 offset:5120
	ds_read_b128 v[26:29], v38 offset:6144
	ds_read_b128 v[30:33], v38 offset:7168
	s_waitcnt lgkmcnt(0)
	s_barrier
	s_mov_b32 m0, s35
	s_nop 0
	global_load_lds_dwordx4 v34, s[16:17] nt
	global_load_lds_dwordx4 v34, s[16:17] offset:1024 nt
	global_load_lds_dwordx4 v34, s[16:17] offset:2048 nt
	global_load_lds_dwordx4 v35, s[16:17] offset:3072 nt
	s_add_u32 s16, s16, 0x7d00
	s_addc_u32 s17, s17, 0
	v_cndmask_b32_e64 v30, 0, v30, s[18:19]
	v_cndmask_b32_e64 v31, 0, v31, s[18:19]
	v_cndmask_b32_e64 v32, 0, v32, s[18:19]
	v_cndmask_b32_e64 v33, 0, v33, s[18:19]
	v_max3_f32 v41, |v18|, |v19|, |v20|
	v_max3_f32 v42, |v21|, |v22|, |v23|
	v_max3_f32 v43, |v24|, |v25|, |v26|
	v_max3_f32 v44, |v27|, |v28|, |v29|
	v_max3_f32 v48, |v30|, |v31|, |v32|
	v_max3_f32 v41, v41, v42, |v33|
	v_max3_f32 v43, v43, v44, v48
	v_max_f32_e32 v41, v41, v43
	v_pk_add_f32 v[2:3], v[2:3], v[18:19]
	v_pk_add_f32 v[4:5], v[4:5], v[20:21]
	v_max_f32_dpp v41, v41, v41 quad_perm:[1,0,3,2] row_mask:0xf bank_mask:0xf
	v_pk_add_f32 v[6:7], v[6:7], v[22:23]
	v_pk_add_f32 v[8:9], v[8:9], v[24:25]
	v_max_f32_dpp v41, v41, v41 quad_perm:[2,3,0,1] row_mask:0xf bank_mask:0xf
	v_pk_add_f32 v[10:11], v[10:11], v[26:27]
	v_pk_add_f32 v[12:13], v[12:13], v[28:29]
	v_max_f32_dpp v41, v41, v41 row_half_mirror row_mask:0xf bank_mask:0xf
	v_pk_add_f32 v[14:15], v[14:15], v[30:31]
	v_pk_add_f32 v[16:17], v[16:17], v[32:33]
	v_max_f32_dpp v41, v41, v41 row_mirror row_mask:0xf bank_mask:0xf
	s_nop 1
	v_max_f32_dpp v41, v41, v41 row_bcast:15 row_mask:0xa bank_mask:0xf
	s_nop 1
	v_max_f32_dpp v41, v41, v41 row_bcast:31 row_mask:0xc bank_mask:0xf
	s_nop 1
	v_readlane_b32 s28, v41, 63
	s_nop 1
	v_div_scale_f32 v48, s[30:31], s28, s28, v47
	v_rcp_f32_e32 v49, v48
	s_nop 0
	v_fma_f32 v50, -v48, v49, 1.0
	v_fmac_f32_e32 v49, v50, v49
	v_mov_b32_e32 v50, s28
	v_div_scale_f32 v50, vcc, s32, v50, s32
	v_mul_f32_e32 v51, v50, v49
	v_fma_f32 v52, -v48, v51, v50
	v_fmac_f32_e32 v51, v52, v49
	v_fma_f32 v48, -v48, v51, v50
	v_div_fmas_f32 v48, v48, v49, v51
	v_div_fixup_f32 v48, v48, s28, v47
	v_cmp_gt_f32_e64 vcc, s28, 0
	v_writelane_b32 v40, s28, 3
	s_nop 0
	v_cndmask_b32_e32 v48, 0, v48, vcc
	v_fmaak_f32 v49, v18, v48, 0x4b400000
	v_fmaak_f32 v50, v19, v48, 0x4b400000
	v_fmaak_f32 v51, v20, v48, 0x4b400000
	v_fmaak_f32 v52, v21, v48, 0x4b400000
	v_perm_b32 v49, v50, v49, s33
	v_perm_b32 v51, v52, v51, s34
	v_or_b32_e32 v68, v49, v51
	v_fmaak_f32 v41, v22, v48, 0x4b400000
	v_fmaak_f32 v42, v23, v48, 0x4b400000
	v_fmaak_f32 v43, v24, v48, 0x4b400000
	v_fmaak_f32 v44, v25, v48, 0x4b400000
	v_perm_b32 v41, v42, v41, s33
	v_perm_b32 v43, v44, v43, s34
	v_or_b32_e32 v69, v41, v43
	v_fmaak_f32 v49, v26, v48, 0x4b400000
	v_fmaak_f32 v50, v27, v48, 0x4b400000
	v_fmaak_f32 v51, v28, v48, 0x4b400000
	v_fmaak_f32 v52, v29, v48, 0x4b400000
	v_perm_b32 v49, v50, v49, s33
	v_perm_b32 v51, v52, v51, s34
	v_or_b32_e32 v70, v49, v51
	v_fmaak_f32 v41, v30, v48, 0x4b400000
	v_fmaak_f32 v42, v31, v48, 0x4b400000
	v_fmaak_f32 v43, v32, v48, 0x4b400000
	v_fmaak_f32 v44, v33, v48, 0x4b400000
	v_perm_b32 v41, v42, v41, s33
	v_perm_b32 v43, v44, v43, s34
	v_or_b32_e32 v71, v41, v43
	s_waitcnt vmcnt(0)
	ds_read_b128 v[18:21], v38 offset:0
	ds_read_b128 v[22:25], v38 offset:1024
	ds_read_b128 v[26:29], v38 offset:2048
	ds_read_b128 v[30:33], v38 offset:3072
	s_waitcnt lgkmcnt(0)
	s_barrier
	s_mov_b32 m0, s36
	s_nop 0
	global_load_lds_dwordx4 v34, s[16:17] nt
	global_load_lds_dwordx4 v34, s[16:17] offset:1024 nt
	global_load_lds_dwordx4 v34, s[16:17] offset:2048 nt
	global_load_lds_dwordx4 v35, s[16:17] offset:3072 nt
	s_add_u32 s16, s16, 0x7d00
	s_addc_u32 s17, s17, 0
	v_cndmask_b32_e64 v30, 0, v30, s[18:19]
	v_cndmask_b32_e64 v31, 0, v31, s[18:19]
	v_cndmask_b32_e64 v32, 0, v32, s[18:19]
	v_cndmask_b32_e64 v33, 0, v33, s[18:19]
	v_max3_f32 v41, |v18|, |v19|, |v20|
	v_max3_f32 v42, |v21|, |v22|, |v23|
	v_max3_f32 v43, |v24|, |v25|, |v26|
	v_max3_f32 v44, |v27|, |v28|, |v29|
	v_max3_f32 v48, |v30|, |v31|, |v32|
	v_max3_f32 v41, v41, v42, |v33|
	v_max3_f32 v43, v43, v44, v48
	v_max_f32_e32 v41, v41, v43
	v_pk_add_f32 v[2:3], v[2:3], v[18:19]
	v_pk_add_f32 v[4:5], v[4:5], v[20:21]
	v_max_f32_dpp v41, v41, v41 quad_perm:[1,0,3,2] row_mask:0xf bank_mask:0xf
	v_pk_add_f32 v[6:7], v[6:7], v[22:23]
	v_pk_add_f32 v[8:9], v[8:9], v[24:25]
	v_max_f32_dpp v41, v41, v41 quad_perm:[2,3,0,1] row_mask:0xf bank_mask:0xf
	v_pk_add_f32 v[10:11], v[10:11], v[26:27]
	v_pk_add_f32 v[12:13], v[12:13], v[28:29]
	v_max_f32_dpp v41, v41, v41 row_half_mirror row_mask:0xf bank_mask:0xf
	v_pk_add_f32 v[14:15], v[14:15], v[30:31]
	v_pk_add_f32 v[16:17], v[16:17], v[32:33]
	v_max_f32_dpp v41, v41, v41 row_mirror row_mask:0xf bank_mask:0xf
	s_nop 1
	v_max_f32_dpp v41, v41, v41 row_bcast:15 row_mask:0xa bank_mask:0xf
	s_nop 1
	v_max_f32_dpp v41, v41, v41 row_bcast:31 row_mask:0xc bank_mask:0xf
	s_nop 1
	v_readlane_b32 s28, v41, 63
	s_nop 1
	v_div_scale_f32 v48, s[30:31], s28, s28, v47
	v_rcp_f32_e32 v49, v48
	s_nop 0
	v_fma_f32 v50, -v48, v49, 1.0
	v_fmac_f32_e32 v49, v50, v49
	v_mov_b32_e32 v50, s28
	v_div_scale_f32 v50, vcc, s32, v50, s32
	v_mul_f32_e32 v51, v50, v49
	v_fma_f32 v52, -v48, v51, v50
	v_fmac_f32_e32 v51, v52, v49
	v_fma_f32 v48, -v48, v51, v50
	v_div_fmas_f32 v48, v48, v49, v51
	v_div_fixup_f32 v48, v48, s28, v47
	v_cmp_gt_f32_e64 vcc, s28, 0
	v_writelane_b32 v40, s28, 4
	s_nop 0
	v_cndmask_b32_e32 v48, 0, v48, vcc
	v_fmaak_f32 v49, v18, v48, 0x4b400000
	v_fmaak_f32 v50, v19, v48, 0x4b400000
	v_fmaak_f32 v51, v20, v48, 0x4b400000
	v_fmaak_f32 v52, v21, v48, 0x4b400000
	v_perm_b32 v49, v50, v49, s33
	v_perm_b32 v51, v52, v51, s34
	v_or_b32_e32 v72, v49, v51
	v_fmaak_f32 v41, v22, v48, 0x4b400000
	v_fmaak_f32 v42, v23, v48, 0x4b400000
	v_fmaak_f32 v43, v24, v48, 0x4b400000
	v_fmaak_f32 v44, v25, v48, 0x4b400000
	v_perm_b32 v41, v42, v41, s33
	v_perm_b32 v43, v44, v43, s34
	v_or_b32_e32 v73, v41, v43
	v_fmaak_f32 v49, v26, v48, 0x4b400000
	v_fmaak_f32 v50, v27, v48, 0x4b400000
	v_fmaak_f32 v51, v28, v48, 0x4b400000
	v_fmaak_f32 v52, v29, v48, 0x4b400000
	v_perm_b32 v49, v50, v49, s33
	v_perm_b32 v51, v52, v51, s34
	v_or_b32_e32 v74, v49, v51
	v_fmaak_f32 v41, v30, v48, 0x4b400000
	v_fmaak_f32 v42, v31, v48, 0x4b400000
	v_fmaak_f32 v43, v32, v48, 0x4b400000
	v_fmaak_f32 v44, v33, v48, 0x4b400000
	v_perm_b32 v41, v42, v41, s33
	v_perm_b32 v43, v44, v43, s34
	v_or_b32_e32 v75, v41, v43
	s_waitcnt vmcnt(0)
	ds_read_b128 v[18:21], v38 offset:4096
	ds_read_b128 v[22:25], v38 offset:5120
	ds_read_b128 v[26:29], v38 offset:6144
	ds_read_b128 v[30:33], v38 offset:7168
	s_waitcnt lgkmcnt(0)
	s_barrier
	s_mov_b32 m0, s35
	s_nop 0
	global_load_lds_dwordx4 v34, s[16:17] nt
	global_load_lds_dwordx4 v34, s[16:17] offset:1024 nt
	global_load_lds_dwordx4 v34, s[16:17] offset:2048 nt
	global_load_lds_dwordx4 v35, s[16:17] offset:3072 nt
	s_add_u32 s16, s16, 0x7d00
	s_addc_u32 s17, s17, 0
	v_cndmask_b32_e64 v30, 0, v30, s[18:19]
	v_cndmask_b32_e64 v31, 0, v31, s[18:19]
	v_cndmask_b32_e64 v32, 0, v32, s[18:19]
	v_cndmask_b32_e64 v33, 0, v33, s[18:19]
	v_max3_f32 v41, |v18|, |v19|, |v20|
	v_max3_f32 v42, |v21|, |v22|, |v23|
	v_max3_f32 v43, |v24|, |v25|, |v26|
	v_max3_f32 v44, |v27|, |v28|, |v29|
	v_max3_f32 v48, |v30|, |v31|, |v32|
	v_max3_f32 v41, v41, v42, |v33|
	v_max3_f32 v43, v43, v44, v48
	v_max_f32_e32 v41, v41, v43
	v_pk_add_f32 v[2:3], v[2:3], v[18:19]
	v_pk_add_f32 v[4:5], v[4:5], v[20:21]
	v_max_f32_dpp v41, v41, v41 quad_perm:[1,0,3,2] row_mask:0xf bank_mask:0xf
	v_pk_add_f32 v[6:7], v[6:7], v[22:23]
	v_pk_add_f32 v[8:9], v[8:9], v[24:25]
	v_max_f32_dpp v41, v41, v41 quad_perm:[2,3,0,1] row_mask:0xf bank_mask:0xf
	v_pk_add_f32 v[10:11], v[10:11], v[26:27]
	v_pk_add_f32 v[12:13], v[12:13], v[28:29]
	v_max_f32_dpp v41, v41, v41 row_half_mirror row_mask:0xf bank_mask:0xf
	v_pk_add_f32 v[14:15], v[14:15], v[30:31]
	v_pk_add_f32 v[16:17], v[16:17], v[32:33]
	v_max_f32_dpp v41, v41, v41 row_mirror row_mask:0xf bank_mask:0xf
	s_nop 1
	v_max_f32_dpp v41, v41, v41 row_bcast:15 row_mask:0xa bank_mask:0xf
	s_nop 1
	v_max_f32_dpp v41, v41, v41 row_bcast:31 row_mask:0xc bank_mask:0xf
	s_nop 1
	v_readlane_b32 s28, v41, 63
	s_nop 1
	v_div_scale_f32 v48, s[30:31], s28, s28, v47
	v_rcp_f32_e32 v49, v48
	s_nop 0
	v_fma_f32 v50, -v48, v49, 1.0
	v_fmac_f32_e32 v49, v50, v49
	v_mov_b32_e32 v50, s28
	v_div_scale_f32 v50, vcc, s32, v50, s32
	v_mul_f32_e32 v51, v50, v49
	v_fma_f32 v52, -v48, v51, v50
	v_fmac_f32_e32 v51, v52, v49
	v_fma_f32 v48, -v48, v51, v50
	v_div_fmas_f32 v48, v48, v49, v51
	v_div_fixup_f32 v48, v48, s28, v47
	v_cmp_gt_f32_e64 vcc, s28, 0
	v_writelane_b32 v40, s28, 5
	s_nop 0
	v_cndmask_b32_e32 v48, 0, v48, vcc
	v_fmaak_f32 v49, v18, v48, 0x4b400000
	v_fmaak_f32 v50, v19, v48, 0x4b400000
	v_fmaak_f32 v51, v20, v48, 0x4b400000
	v_fmaak_f32 v52, v21, v48, 0x4b400000
	v_perm_b32 v49, v50, v49, s33
	v_perm_b32 v51, v52, v51, s34
	v_or_b32_e32 v76, v49, v51
	v_fmaak_f32 v41, v22, v48, 0x4b400000
	v_fmaak_f32 v42, v23, v48, 0x4b400000
	v_fmaak_f32 v43, v24, v48, 0x4b400000
	v_fmaak_f32 v44, v25, v48, 0x4b400000
	v_perm_b32 v41, v42, v41, s33
	v_perm_b32 v43, v44, v43, s34
	v_or_b32_e32 v77, v41, v43
	v_fmaak_f32 v49, v26, v48, 0x4b400000
	v_fmaak_f32 v50, v27, v48, 0x4b400000
	v_fmaak_f32 v51, v28, v48, 0x4b400000
	v_fmaak_f32 v52, v29, v48, 0x4b400000
	v_perm_b32 v49, v50, v49, s33
	v_perm_b32 v51, v52, v51, s34
	v_or_b32_e32 v78, v49, v51
	v_fmaak_f32 v41, v30, v48, 0x4b400000
	v_fmaak_f32 v42, v31, v48, 0x4b400000
	v_fmaak_f32 v43, v32, v48, 0x4b400000
	v_fmaak_f32 v44, v33, v48, 0x4b400000
	v_perm_b32 v41, v42, v41, s33
	v_perm_b32 v43, v44, v43, s34
	v_or_b32_e32 v79, v41, v43
	s_waitcnt vmcnt(0)
	ds_read_b128 v[18:21], v38 offset:0
	ds_read_b128 v[22:25], v38 offset:1024
	ds_read_b128 v[26:29], v38 offset:2048
	ds_read_b128 v[30:33], v38 offset:3072
	s_waitcnt lgkmcnt(0)
	s_barrier
	s_mov_b32 m0, s36
	s_nop 0
	global_load_lds_dwordx4 v34, s[16:17] nt
	global_load_lds_dwordx4 v34, s[16:17] offset:1024 nt
	global_load_lds_dwordx4 v34, s[16:17] offset:2048 nt
	global_load_lds_dwordx4 v35, s[16:17] offset:3072 nt
	s_add_u32 s16, s16, 0x7d00
	s_addc_u32 s17, s17, 0
	v_cndmask_b32_e64 v30, 0, v30, s[18:19]
	v_cndmask_b32_e64 v31, 0, v31, s[18:19]
	v_cndmask_b32_e64 v32, 0, v32, s[18:19]
	v_cndmask_b32_e64 v33, 0, v33, s[18:19]
	v_max3_f32 v41, |v18|, |v19|, |v20|
	v_max3_f32 v42, |v21|, |v22|, |v23|
	v_max3_f32 v43, |v24|, |v25|, |v26|
	v_max3_f32 v44, |v27|, |v28|, |v29|
	v_max3_f32 v48, |v30|, |v31|, |v32|
	v_max3_f32 v41, v41, v42, |v33|
	v_max3_f32 v43, v43, v44, v48
	v_max_f32_e32 v41, v41, v43
	v_pk_add_f32 v[2:3], v[2:3], v[18:19]
	v_pk_add_f32 v[4:5], v[4:5], v[20:21]
	v_max_f32_dpp v41, v41, v41 quad_perm:[1,0,3,2] row_mask:0xf bank_mask:0xf
	v_pk_add_f32 v[6:7], v[6:7], v[22:23]
	v_pk_add_f32 v[8:9], v[8:9], v[24:25]
	v_max_f32_dpp v41, v41, v41 quad_perm:[2,3,0,1] row_mask:0xf bank_mask:0xf
	v_pk_add_f32 v[10:11], v[10:11], v[26:27]
	v_pk_add_f32 v[12:13], v[12:13], v[28:29]
	v_max_f32_dpp v41, v41, v41 row_half_mirror row_mask:0xf bank_mask:0xf
	v_pk_add_f32 v[14:15], v[14:15], v[30:31]
	v_pk_add_f32 v[16:17], v[16:17], v[32:33]
	v_max_f32_dpp v41, v41, v41 row_mirror row_mask:0xf bank_mask:0xf
	s_nop 1
	v_max_f32_dpp v41, v41, v41 row_bcast:15 row_mask:0xa bank_mask:0xf
	s_nop 1
	v_max_f32_dpp v41, v41, v41 row_bcast:31 row_mask:0xc bank_mask:0xf
	s_nop 1
	v_readlane_b32 s28, v41, 63
	s_nop 1
	v_div_scale_f32 v48, s[30:31], s28, s28, v47
	v_rcp_f32_e32 v49, v48
	s_nop 0
	v_fma_f32 v50, -v48, v49, 1.0
	v_fmac_f32_e32 v49, v50, v49
	v_mov_b32_e32 v50, s28
	v_div_scale_f32 v50, vcc, s32, v50, s32
	v_mul_f32_e32 v51, v50, v49
	v_fma_f32 v52, -v48, v51, v50
	v_fmac_f32_e32 v51, v52, v49
	v_fma_f32 v48, -v48, v51, v50
	v_div_fmas_f32 v48, v48, v49, v51
	v_div_fixup_f32 v48, v48, s28, v47
	v_cmp_gt_f32_e64 vcc, s28, 0
	v_writelane_b32 v40, s28, 6
	s_nop 0
	v_cndmask_b32_e32 v48, 0, v48, vcc
	v_fmaak_f32 v49, v18, v48, 0x4b400000
	v_fmaak_f32 v50, v19, v48, 0x4b400000
	v_fmaak_f32 v51, v20, v48, 0x4b400000
	v_fmaak_f32 v52, v21, v48, 0x4b400000
	v_perm_b32 v49, v50, v49, s33
	v_perm_b32 v51, v52, v51, s34
	v_or_b32_e32 v80, v49, v51
	v_fmaak_f32 v41, v22, v48, 0x4b400000
	v_fmaak_f32 v42, v23, v48, 0x4b400000
	v_fmaak_f32 v43, v24, v48, 0x4b400000
	v_fmaak_f32 v44, v25, v48, 0x4b400000
	v_perm_b32 v41, v42, v41, s33
	v_perm_b32 v43, v44, v43, s34
	v_or_b32_e32 v81, v41, v43
	v_fmaak_f32 v49, v26, v48, 0x4b400000
	v_fmaak_f32 v50, v27, v48, 0x4b400000
	v_fmaak_f32 v51, v28, v48, 0x4b400000
	v_fmaak_f32 v52, v29, v48, 0x4b400000
	v_perm_b32 v49, v50, v49, s33
	v_perm_b32 v51, v52, v51, s34
	v_or_b32_e32 v82, v49, v51
	v_fmaak_f32 v41, v30, v48, 0x4b400000
	v_fmaak_f32 v42, v31, v48, 0x4b400000
	v_fmaak_f32 v43, v32, v48, 0x4b400000
	v_fmaak_f32 v44, v33, v48, 0x4b400000
	v_perm_b32 v41, v42, v41, s33
	v_perm_b32 v43, v44, v43, s34
	v_or_b32_e32 v83, v41, v43
	s_waitcnt vmcnt(0)
	ds_read_b128 v[18:21], v38 offset:4096
	ds_read_b128 v[22:25], v38 offset:5120
	ds_read_b128 v[26:29], v38 offset:6144
	ds_read_b128 v[30:33], v38 offset:7168
	s_waitcnt lgkmcnt(0)
	s_barrier
	s_mov_b32 m0, s35
	s_nop 0
	global_load_lds_dwordx4 v34, s[16:17] nt
	global_load_lds_dwordx4 v34, s[16:17] offset:1024 nt
	global_load_lds_dwordx4 v34, s[16:17] offset:2048 nt
	global_load_lds_dwordx4 v35, s[16:17] offset:3072 nt
	s_add_u32 s16, s16, 0x7d00
	s_addc_u32 s17, s17, 0
	v_cndmask_b32_e64 v30, 0, v30, s[18:19]
	v_cndmask_b32_e64 v31, 0, v31, s[18:19]
	v_cndmask_b32_e64 v32, 0, v32, s[18:19]
	v_cndmask_b32_e64 v33, 0, v33, s[18:19]
	v_max3_f32 v41, |v18|, |v19|, |v20|
	v_max3_f32 v42, |v21|, |v22|, |v23|
	v_max3_f32 v43, |v24|, |v25|, |v26|
	v_max3_f32 v44, |v27|, |v28|, |v29|
	v_max3_f32 v48, |v30|, |v31|, |v32|
	v_max3_f32 v41, v41, v42, |v33|
	v_max3_f32 v43, v43, v44, v48
	v_max_f32_e32 v41, v41, v43
	v_pk_add_f32 v[2:3], v[2:3], v[18:19]
	v_pk_add_f32 v[4:5], v[4:5], v[20:21]
	v_max_f32_dpp v41, v41, v41 quad_perm:[1,0,3,2] row_mask:0xf bank_mask:0xf
	v_pk_add_f32 v[6:7], v[6:7], v[22:23]
	v_pk_add_f32 v[8:9], v[8:9], v[24:25]
	v_max_f32_dpp v41, v41, v41 quad_perm:[2,3,0,1] row_mask:0xf bank_mask:0xf
	v_pk_add_f32 v[10:11], v[10:11], v[26:27]
	v_pk_add_f32 v[12:13], v[12:13], v[28:29]
	v_max_f32_dpp v41, v41, v41 row_half_mirror row_mask:0xf bank_mask:0xf
	v_pk_add_f32 v[14:15], v[14:15], v[30:31]
	v_pk_add_f32 v[16:17], v[16:17], v[32:33]
	v_max_f32_dpp v41, v41, v41 row_mirror row_mask:0xf bank_mask:0xf
	s_nop 1
	v_max_f32_dpp v41, v41, v41 row_bcast:15 row_mask:0xa bank_mask:0xf
	s_nop 1
	v_max_f32_dpp v41, v41, v41 row_bcast:31 row_mask:0xc bank_mask:0xf
	s_nop 1
	v_readlane_b32 s28, v41, 63
	s_nop 1
	v_div_scale_f32 v48, s[30:31], s28, s28, v47
	v_rcp_f32_e32 v49, v48
	s_nop 0
	v_fma_f32 v50, -v48, v49, 1.0
	v_fmac_f32_e32 v49, v50, v49
	v_mov_b32_e32 v50, s28
	v_div_scale_f32 v50, vcc, s32, v50, s32
	v_mul_f32_e32 v51, v50, v49
	v_fma_f32 v52, -v48, v51, v50
	v_fmac_f32_e32 v51, v52, v49
	v_fma_f32 v48, -v48, v51, v50
	v_div_fmas_f32 v48, v48, v49, v51
	v_div_fixup_f32 v48, v48, s28, v47
	v_cmp_gt_f32_e64 vcc, s28, 0
	v_writelane_b32 v40, s28, 7
	s_nop 0
	v_cndmask_b32_e32 v48, 0, v48, vcc
	v_fmaak_f32 v49, v18, v48, 0x4b400000
	v_fmaak_f32 v50, v19, v48, 0x4b400000
	v_fmaak_f32 v51, v20, v48, 0x4b400000
	v_fmaak_f32 v52, v21, v48, 0x4b400000
	v_perm_b32 v49, v50, v49, s33
	v_perm_b32 v51, v52, v51, s34
	v_or_b32_e32 v84, v49, v51
	v_fmaak_f32 v41, v22, v48, 0x4b400000
	v_fmaak_f32 v42, v23, v48, 0x4b400000
	v_fmaak_f32 v43, v24, v48, 0x4b400000
	v_fmaak_f32 v44, v25, v48, 0x4b400000
	v_perm_b32 v41, v42, v41, s33
	v_perm_b32 v43, v44, v43, s34
	v_or_b32_e32 v85, v41, v43
	v_fmaak_f32 v49, v26, v48, 0x4b400000
	v_fmaak_f32 v50, v27, v48, 0x4b400000
	v_fmaak_f32 v51, v28, v48, 0x4b400000
	v_fmaak_f32 v52, v29, v48, 0x4b400000
	v_perm_b32 v49, v50, v49, s33
	v_perm_b32 v51, v52, v51, s34
	v_or_b32_e32 v86, v49, v51
	v_fmaak_f32 v41, v30, v48, 0x4b400000
	v_fmaak_f32 v42, v31, v48, 0x4b400000
	v_fmaak_f32 v43, v32, v48, 0x4b400000
	v_fmaak_f32 v44, v33, v48, 0x4b400000
	v_perm_b32 v41, v42, v41, s33
	v_perm_b32 v43, v44, v43, s34
	v_or_b32_e32 v87, v41, v43
	s_waitcnt vmcnt(0)
	ds_read_b128 v[18:21], v38 offset:0
	ds_read_b128 v[22:25], v38 offset:1024
	ds_read_b128 v[26:29], v38 offset:2048
	ds_read_b128 v[30:33], v38 offset:3072
	s_waitcnt lgkmcnt(0)
	s_barrier
	s_mov_b32 m0, s36
	s_nop 0
	global_load_lds_dwordx4 v34, s[16:17] nt
	global_load_lds_dwordx4 v34, s[16:17] offset:1024 nt
	global_load_lds_dwordx4 v34, s[16:17] offset:2048 nt
	global_load_lds_dwordx4 v35, s[16:17] offset:3072 nt
	s_add_u32 s16, s16, 0x7d00
	s_addc_u32 s17, s17, 0
	v_cndmask_b32_e64 v30, 0, v30, s[18:19]
	v_cndmask_b32_e64 v31, 0, v31, s[18:19]
	v_cndmask_b32_e64 v32, 0, v32, s[18:19]
	v_cndmask_b32_e64 v33, 0, v33, s[18:19]
	v_max3_f32 v41, |v18|, |v19|, |v20|
	v_max3_f32 v42, |v21|, |v22|, |v23|
	v_max3_f32 v43, |v24|, |v25|, |v26|
	v_max3_f32 v44, |v27|, |v28|, |v29|
	v_max3_f32 v48, |v30|, |v31|, |v32|
	v_max3_f32 v41, v41, v42, |v33|
	v_max3_f32 v43, v43, v44, v48
	v_max_f32_e32 v41, v41, v43
	v_pk_add_f32 v[2:3], v[2:3], v[18:19]
	v_pk_add_f32 v[4:5], v[4:5], v[20:21]
	v_max_f32_dpp v41, v41, v41 quad_perm:[1,0,3,2] row_mask:0xf bank_mask:0xf
	v_pk_add_f32 v[6:7], v[6:7], v[22:23]
	v_pk_add_f32 v[8:9], v[8:9], v[24:25]
	v_max_f32_dpp v41, v41, v41 quad_perm:[2,3,0,1] row_mask:0xf bank_mask:0xf
	v_pk_add_f32 v[10:11], v[10:11], v[26:27]
	v_pk_add_f32 v[12:13], v[12:13], v[28:29]
	v_max_f32_dpp v41, v41, v41 row_half_mirror row_mask:0xf bank_mask:0xf
	v_pk_add_f32 v[14:15], v[14:15], v[30:31]
	v_pk_add_f32 v[16:17], v[16:17], v[32:33]
	v_max_f32_dpp v41, v41, v41 row_mirror row_mask:0xf bank_mask:0xf
	s_nop 1
	v_max_f32_dpp v41, v41, v41 row_bcast:15 row_mask:0xa bank_mask:0xf
	s_nop 1
	v_max_f32_dpp v41, v41, v41 row_bcast:31 row_mask:0xc bank_mask:0xf
	s_nop 1
	v_readlane_b32 s28, v41, 63
	s_nop 1
	v_div_scale_f32 v48, s[30:31], s28, s28, v47
	v_rcp_f32_e32 v49, v48
	s_nop 0
	v_fma_f32 v50, -v48, v49, 1.0
	v_fmac_f32_e32 v49, v50, v49
	v_mov_b32_e32 v50, s28
	v_div_scale_f32 v50, vcc, s32, v50, s32
	v_mul_f32_e32 v51, v50, v49
	v_fma_f32 v52, -v48, v51, v50
	v_fmac_f32_e32 v51, v52, v49
	v_fma_f32 v48, -v48, v51, v50
	v_div_fmas_f32 v48, v48, v49, v51
	v_div_fixup_f32 v48, v48, s28, v47
	v_cmp_gt_f32_e64 vcc, s28, 0
	v_writelane_b32 v40, s28, 8
	s_nop 0
	v_cndmask_b32_e32 v48, 0, v48, vcc
	v_fmaak_f32 v49, v18, v48, 0x4b400000
	v_fmaak_f32 v50, v19, v48, 0x4b400000
	v_fmaak_f32 v51, v20, v48, 0x4b400000
	v_fmaak_f32 v52, v21, v48, 0x4b400000
	v_perm_b32 v49, v50, v49, s33
	v_perm_b32 v51, v52, v51, s34
	v_or_b32_e32 v88, v49, v51
	v_fmaak_f32 v41, v22, v48, 0x4b400000
	v_fmaak_f32 v42, v23, v48, 0x4b400000
	v_fmaak_f32 v43, v24, v48, 0x4b400000
	v_fmaak_f32 v44, v25, v48, 0x4b400000
	v_perm_b32 v41, v42, v41, s33
	v_perm_b32 v43, v44, v43, s34
	v_or_b32_e32 v89, v41, v43
	v_fmaak_f32 v49, v26, v48, 0x4b400000
	v_fmaak_f32 v50, v27, v48, 0x4b400000
	v_fmaak_f32 v51, v28, v48, 0x4b400000
	v_fmaak_f32 v52, v29, v48, 0x4b400000
	v_perm_b32 v49, v50, v49, s33
	v_perm_b32 v51, v52, v51, s34
	v_or_b32_e32 v90, v49, v51
	v_fmaak_f32 v41, v30, v48, 0x4b400000
	v_fmaak_f32 v42, v31, v48, 0x4b400000
	v_fmaak_f32 v43, v32, v48, 0x4b400000
	v_fmaak_f32 v44, v33, v48, 0x4b400000
	v_perm_b32 v41, v42, v41, s33
	v_perm_b32 v43, v44, v43, s34
	v_or_b32_e32 v91, v41, v43
	s_waitcnt vmcnt(0)
	ds_read_b128 v[18:21], v38 offset:4096
	ds_read_b128 v[22:25], v38 offset:5120
	ds_read_b128 v[26:29], v38 offset:6144
	ds_read_b128 v[30:33], v38 offset:7168
	s_waitcnt lgkmcnt(0)
	s_barrier
	s_mov_b32 m0, s35
	s_nop 0
	global_load_lds_dwordx4 v34, s[16:17] nt
	global_load_lds_dwordx4 v34, s[16:17] offset:1024 nt
	global_load_lds_dwordx4 v34, s[16:17] offset:2048 nt
	global_load_lds_dwordx4 v35, s[16:17] offset:3072 nt
	s_add_u32 s16, s16, 0x7d00
	s_addc_u32 s17, s17, 0
	v_cndmask_b32_e64 v30, 0, v30, s[18:19]
	v_cndmask_b32_e64 v31, 0, v31, s[18:19]
	v_cndmask_b32_e64 v32, 0, v32, s[18:19]
	v_cndmask_b32_e64 v33, 0, v33, s[18:19]
	v_max3_f32 v41, |v18|, |v19|, |v20|
	v_max3_f32 v42, |v21|, |v22|, |v23|
	v_max3_f32 v43, |v24|, |v25|, |v26|
	v_max3_f32 v44, |v27|, |v28|, |v29|
	v_max3_f32 v48, |v30|, |v31|, |v32|
	v_max3_f32 v41, v41, v42, |v33|
	v_max3_f32 v43, v43, v44, v48
	v_max_f32_e32 v41, v41, v43
	v_pk_add_f32 v[2:3], v[2:3], v[18:19]
	v_pk_add_f32 v[4:5], v[4:5], v[20:21]
	v_max_f32_dpp v41, v41, v41 quad_perm:[1,0,3,2] row_mask:0xf bank_mask:0xf
	v_pk_add_f32 v[6:7], v[6:7], v[22:23]
	v_pk_add_f32 v[8:9], v[8:9], v[24:25]
	v_max_f32_dpp v41, v41, v41 quad_perm:[2,3,0,1] row_mask:0xf bank_mask:0xf
	v_pk_add_f32 v[10:11], v[10:11], v[26:27]
	v_pk_add_f32 v[12:13], v[12:13], v[28:29]
	v_max_f32_dpp v41, v41, v41 row_half_mirror row_mask:0xf bank_mask:0xf
	v_pk_add_f32 v[14:15], v[14:15], v[30:31]
	v_pk_add_f32 v[16:17], v[16:17], v[32:33]
	v_max_f32_dpp v41, v41, v41 row_mirror row_mask:0xf bank_mask:0xf
	s_nop 1
	v_max_f32_dpp v41, v41, v41 row_bcast:15 row_mask:0xa bank_mask:0xf
	s_nop 1
	v_max_f32_dpp v41, v41, v41 row_bcast:31 row_mask:0xc bank_mask:0xf
	s_nop 1
	v_readlane_b32 s28, v41, 63
	s_nop 1
	v_div_scale_f32 v48, s[30:31], s28, s28, v47
	v_rcp_f32_e32 v49, v48
	s_nop 0
	v_fma_f32 v50, -v48, v49, 1.0
	v_fmac_f32_e32 v49, v50, v49
	v_mov_b32_e32 v50, s28
	v_div_scale_f32 v50, vcc, s32, v50, s32
	v_mul_f32_e32 v51, v50, v49
	v_fma_f32 v52, -v48, v51, v50
	v_fmac_f32_e32 v51, v52, v49
	v_fma_f32 v48, -v48, v51, v50
	v_div_fmas_f32 v48, v48, v49, v51
	v_div_fixup_f32 v48, v48, s28, v47
	v_cmp_gt_f32_e64 vcc, s28, 0
	v_writelane_b32 v40, s28, 9
	s_nop 0
	v_cndmask_b32_e32 v48, 0, v48, vcc
	v_fmaak_f32 v49, v18, v48, 0x4b400000
	v_fmaak_f32 v50, v19, v48, 0x4b400000
	v_fmaak_f32 v51, v20, v48, 0x4b400000
	v_fmaak_f32 v52, v21, v48, 0x4b400000
	v_perm_b32 v49, v50, v49, s33
	v_perm_b32 v51, v52, v51, s34
	v_or_b32_e32 v92, v49, v51
	v_fmaak_f32 v41, v22, v48, 0x4b400000
	v_fmaak_f32 v42, v23, v48, 0x4b400000
	v_fmaak_f32 v43, v24, v48, 0x4b400000
	v_fmaak_f32 v44, v25, v48, 0x4b400000
	v_perm_b32 v41, v42, v41, s33
	v_perm_b32 v43, v44, v43, s34
	v_or_b32_e32 v93, v41, v43
	v_fmaak_f32 v49, v26, v48, 0x4b400000
	v_fmaak_f32 v50, v27, v48, 0x4b400000
	v_fmaak_f32 v51, v28, v48, 0x4b400000
	v_fmaak_f32 v52, v29, v48, 0x4b400000
	v_perm_b32 v49, v50, v49, s33
	v_perm_b32 v51, v52, v51, s34
	v_or_b32_e32 v94, v49, v51
	v_fmaak_f32 v41, v30, v48, 0x4b400000
	v_fmaak_f32 v42, v31, v48, 0x4b400000
	v_fmaak_f32 v43, v32, v48, 0x4b400000
	v_fmaak_f32 v44, v33, v48, 0x4b400000
	v_perm_b32 v41, v42, v41, s33
	v_perm_b32 v43, v44, v43, s34
	v_or_b32_e32 v95, v41, v43
	s_waitcnt vmcnt(0)
	ds_read_b128 v[18:21], v38 offset:0
	ds_read_b128 v[22:25], v38 offset:1024
	ds_read_b128 v[26:29], v38 offset:2048
	ds_read_b128 v[30:33], v38 offset:3072
	s_waitcnt lgkmcnt(0)
	s_barrier
	s_mov_b32 m0, s36
	s_nop 0
	global_load_lds_dwordx4 v34, s[16:17] nt
	global_load_lds_dwordx4 v34, s[16:17] offset:1024 nt
	global_load_lds_dwordx4 v34, s[16:17] offset:2048 nt
	global_load_lds_dwordx4 v35, s[16:17] offset:3072 nt
	s_add_u32 s16, s16, 0x7d00
	s_addc_u32 s17, s17, 0
	v_cndmask_b32_e64 v30, 0, v30, s[18:19]
	v_cndmask_b32_e64 v31, 0, v31, s[18:19]
	v_cndmask_b32_e64 v32, 0, v32, s[18:19]
	v_cndmask_b32_e64 v33, 0, v33, s[18:19]
	v_max3_f32 v41, |v18|, |v19|, |v20|
	v_max3_f32 v42, |v21|, |v22|, |v23|
	v_max3_f32 v43, |v24|, |v25|, |v26|
	v_max3_f32 v44, |v27|, |v28|, |v29|
	v_max3_f32 v48, |v30|, |v31|, |v32|
	v_max3_f32 v41, v41, v42, |v33|
	v_max3_f32 v43, v43, v44, v48
	v_max_f32_e32 v41, v41, v43
	v_pk_add_f32 v[2:3], v[2:3], v[18:19]
	v_pk_add_f32 v[4:5], v[4:5], v[20:21]
	v_max_f32_dpp v41, v41, v41 quad_perm:[1,0,3,2] row_mask:0xf bank_mask:0xf
	v_pk_add_f32 v[6:7], v[6:7], v[22:23]
	v_pk_add_f32 v[8:9], v[8:9], v[24:25]
	v_max_f32_dpp v41, v41, v41 quad_perm:[2,3,0,1] row_mask:0xf bank_mask:0xf
	v_pk_add_f32 v[10:11], v[10:11], v[26:27]
	v_pk_add_f32 v[12:13], v[12:13], v[28:29]
	v_max_f32_dpp v41, v41, v41 row_half_mirror row_mask:0xf bank_mask:0xf
	v_pk_add_f32 v[14:15], v[14:15], v[30:31]
	v_pk_add_f32 v[16:17], v[16:17], v[32:33]
	v_max_f32_dpp v41, v41, v41 row_mirror row_mask:0xf bank_mask:0xf
	s_nop 1
	v_max_f32_dpp v41, v41, v41 row_bcast:15 row_mask:0xa bank_mask:0xf
	s_nop 1
	v_max_f32_dpp v41, v41, v41 row_bcast:31 row_mask:0xc bank_mask:0xf
	s_nop 1
	v_readlane_b32 s28, v41, 63
	s_nop 1
	v_div_scale_f32 v48, s[30:31], s28, s28, v47
	v_rcp_f32_e32 v49, v48
	s_nop 0
	v_fma_f32 v50, -v48, v49, 1.0
	v_fmac_f32_e32 v49, v50, v49
	v_mov_b32_e32 v50, s28
	v_div_scale_f32 v50, vcc, s32, v50, s32
	v_mul_f32_e32 v51, v50, v49
	v_fma_f32 v52, -v48, v51, v50
	v_fmac_f32_e32 v51, v52, v49
	v_fma_f32 v48, -v48, v51, v50
	v_div_fmas_f32 v48, v48, v49, v51
	v_div_fixup_f32 v48, v48, s28, v47
	v_cmp_gt_f32_e64 vcc, s28, 0
	v_writelane_b32 v40, s28, 10
	s_nop 0
	v_cndmask_b32_e32 v48, 0, v48, vcc
	v_fmaak_f32 v49, v18, v48, 0x4b400000
	v_fmaak_f32 v50, v19, v48, 0x4b400000
	v_fmaak_f32 v51, v20, v48, 0x4b400000
	v_fmaak_f32 v52, v21, v48, 0x4b400000
	v_perm_b32 v49, v50, v49, s33
	v_perm_b32 v51, v52, v51, s34
	v_or_b32_e32 v96, v49, v51
	v_fmaak_f32 v41, v22, v48, 0x4b400000
	v_fmaak_f32 v42, v23, v48, 0x4b400000
	v_fmaak_f32 v43, v24, v48, 0x4b400000
	v_fmaak_f32 v44, v25, v48, 0x4b400000
	v_perm_b32 v41, v42, v41, s33
	v_perm_b32 v43, v44, v43, s34
	v_or_b32_e32 v97, v41, v43
	v_fmaak_f32 v49, v26, v48, 0x4b400000
	v_fmaak_f32 v50, v27, v48, 0x4b400000
	v_fmaak_f32 v51, v28, v48, 0x4b400000
	v_fmaak_f32 v52, v29, v48, 0x4b400000
	v_perm_b32 v49, v50, v49, s33
	v_perm_b32 v51, v52, v51, s34
	v_or_b32_e32 v98, v49, v51
	v_fmaak_f32 v41, v30, v48, 0x4b400000
	v_fmaak_f32 v42, v31, v48, 0x4b400000
	v_fmaak_f32 v43, v32, v48, 0x4b400000
	v_fmaak_f32 v44, v33, v48, 0x4b400000
	v_perm_b32 v41, v42, v41, s33
	v_perm_b32 v43, v44, v43, s34
	v_or_b32_e32 v99, v41, v43
	s_waitcnt vmcnt(0)
	ds_read_b128 v[18:21], v38 offset:4096
	ds_read_b128 v[22:25], v38 offset:5120
	ds_read_b128 v[26:29], v38 offset:6144
	ds_read_b128 v[30:33], v38 offset:7168
	s_waitcnt lgkmcnt(0)
	s_barrier
	s_mov_b32 m0, s35
	s_nop 0
	global_load_lds_dwordx4 v34, s[16:17] nt
	global_load_lds_dwordx4 v34, s[16:17] offset:1024 nt
	global_load_lds_dwordx4 v34, s[16:17] offset:2048 nt
	global_load_lds_dwordx4 v35, s[16:17] offset:3072 nt
	s_add_u32 s16, s16, 0x7d00
	s_addc_u32 s17, s17, 0
	v_cndmask_b32_e64 v30, 0, v30, s[18:19]
	v_cndmask_b32_e64 v31, 0, v31, s[18:19]
	v_cndmask_b32_e64 v32, 0, v32, s[18:19]
	v_cndmask_b32_e64 v33, 0, v33, s[18:19]
	v_max3_f32 v41, |v18|, |v19|, |v20|
	v_max3_f32 v42, |v21|, |v22|, |v23|
	v_max3_f32 v43, |v24|, |v25|, |v26|
	v_max3_f32 v44, |v27|, |v28|, |v29|
	v_max3_f32 v48, |v30|, |v31|, |v32|
	v_max3_f32 v41, v41, v42, |v33|
	v_max3_f32 v43, v43, v44, v48
	v_max_f32_e32 v41, v41, v43
	v_pk_add_f32 v[2:3], v[2:3], v[18:19]
	v_pk_add_f32 v[4:5], v[4:5], v[20:21]
	v_max_f32_dpp v41, v41, v41 quad_perm:[1,0,3,2] row_mask:0xf bank_mask:0xf
	v_pk_add_f32 v[6:7], v[6:7], v[22:23]
	v_pk_add_f32 v[8:9], v[8:9], v[24:25]
	v_max_f32_dpp v41, v41, v41 quad_perm:[2,3,0,1] row_mask:0xf bank_mask:0xf
	v_pk_add_f32 v[10:11], v[10:11], v[26:27]
	v_pk_add_f32 v[12:13], v[12:13], v[28:29]
	v_max_f32_dpp v41, v41, v41 row_half_mirror row_mask:0xf bank_mask:0xf
	v_pk_add_f32 v[14:15], v[14:15], v[30:31]
	v_pk_add_f32 v[16:17], v[16:17], v[32:33]
	v_max_f32_dpp v41, v41, v41 row_mirror row_mask:0xf bank_mask:0xf
	s_nop 1
	v_max_f32_dpp v41, v41, v41 row_bcast:15 row_mask:0xa bank_mask:0xf
	s_nop 1
	v_max_f32_dpp v41, v41, v41 row_bcast:31 row_mask:0xc bank_mask:0xf
	s_nop 1
	v_readlane_b32 s28, v41, 63
	s_nop 1
	v_div_scale_f32 v48, s[30:31], s28, s28, v47
	v_rcp_f32_e32 v49, v48
	s_nop 0
	v_fma_f32 v50, -v48, v49, 1.0
	v_fmac_f32_e32 v49, v50, v49
	v_mov_b32_e32 v50, s28
	v_div_scale_f32 v50, vcc, s32, v50, s32
	v_mul_f32_e32 v51, v50, v49
	v_fma_f32 v52, -v48, v51, v50
	v_fmac_f32_e32 v51, v52, v49
	v_fma_f32 v48, -v48, v51, v50
	v_div_fmas_f32 v48, v48, v49, v51
	v_div_fixup_f32 v48, v48, s28, v47
	v_cmp_gt_f32_e64 vcc, s28, 0
	v_writelane_b32 v40, s28, 11
	s_nop 0
	v_cndmask_b32_e32 v48, 0, v48, vcc
	v_fmaak_f32 v49, v18, v48, 0x4b400000
	v_fmaak_f32 v50, v19, v48, 0x4b400000
	v_fmaak_f32 v51, v20, v48, 0x4b400000
	v_fmaak_f32 v52, v21, v48, 0x4b400000
	v_perm_b32 v49, v50, v49, s33
	v_perm_b32 v51, v52, v51, s34
	v_or_b32_e32 v100, v49, v51
	v_fmaak_f32 v41, v22, v48, 0x4b400000
	v_fmaak_f32 v42, v23, v48, 0x4b400000
	v_fmaak_f32 v43, v24, v48, 0x4b400000
	v_fmaak_f32 v44, v25, v48, 0x4b400000
	v_perm_b32 v41, v42, v41, s33
	v_perm_b32 v43, v44, v43, s34
	v_or_b32_e32 v101, v41, v43
	v_fmaak_f32 v49, v26, v48, 0x4b400000
	v_fmaak_f32 v50, v27, v48, 0x4b400000
	v_fmaak_f32 v51, v28, v48, 0x4b400000
	v_fmaak_f32 v52, v29, v48, 0x4b400000
	v_perm_b32 v49, v50, v49, s33
	v_perm_b32 v51, v52, v51, s34
	v_or_b32_e32 v102, v49, v51
	v_fmaak_f32 v41, v30, v48, 0x4b400000
	v_fmaak_f32 v42, v31, v48, 0x4b400000
	v_fmaak_f32 v43, v32, v48, 0x4b400000
	v_fmaak_f32 v44, v33, v48, 0x4b400000
	v_perm_b32 v41, v42, v41, s33
	v_perm_b32 v43, v44, v43, s34
	v_or_b32_e32 v103, v41, v43
	s_waitcnt vmcnt(0)
	ds_read_b128 v[18:21], v38 offset:0
	ds_read_b128 v[22:25], v38 offset:1024
	ds_read_b128 v[26:29], v38 offset:2048
	ds_read_b128 v[30:33], v38 offset:3072
	s_waitcnt lgkmcnt(0)
	s_barrier
	s_mov_b32 m0, s36
	s_nop 0
	global_load_lds_dwordx4 v34, s[16:17] nt
	global_load_lds_dwordx4 v34, s[16:17] offset:1024 nt
	global_load_lds_dwordx4 v34, s[16:17] offset:2048 nt
	global_load_lds_dwordx4 v35, s[16:17] offset:3072 nt
	s_add_u32 s16, s16, 0x7d00
	s_addc_u32 s17, s17, 0
	v_cndmask_b32_e64 v30, 0, v30, s[18:19]
	v_cndmask_b32_e64 v31, 0, v31, s[18:19]
	v_cndmask_b32_e64 v32, 0, v32, s[18:19]
	v_cndmask_b32_e64 v33, 0, v33, s[18:19]
	v_max3_f32 v41, |v18|, |v19|, |v20|
	v_max3_f32 v42, |v21|, |v22|, |v23|
	v_max3_f32 v43, |v24|, |v25|, |v26|
	v_max3_f32 v44, |v27|, |v28|, |v29|
	v_max3_f32 v48, |v30|, |v31|, |v32|
	v_max3_f32 v41, v41, v42, |v33|
	v_max3_f32 v43, v43, v44, v48
	v_max_f32_e32 v41, v41, v43
	v_pk_add_f32 v[2:3], v[2:3], v[18:19]
	v_pk_add_f32 v[4:5], v[4:5], v[20:21]
	v_max_f32_dpp v41, v41, v41 quad_perm:[1,0,3,2] row_mask:0xf bank_mask:0xf
	v_pk_add_f32 v[6:7], v[6:7], v[22:23]
	v_pk_add_f32 v[8:9], v[8:9], v[24:25]
	v_max_f32_dpp v41, v41, v41 quad_perm:[2,3,0,1] row_mask:0xf bank_mask:0xf
	v_pk_add_f32 v[10:11], v[10:11], v[26:27]
	v_pk_add_f32 v[12:13], v[12:13], v[28:29]
	v_max_f32_dpp v41, v41, v41 row_half_mirror row_mask:0xf bank_mask:0xf
	v_pk_add_f32 v[14:15], v[14:15], v[30:31]
	v_pk_add_f32 v[16:17], v[16:17], v[32:33]
	v_max_f32_dpp v41, v41, v41 row_mirror row_mask:0xf bank_mask:0xf
	s_nop 1
	v_max_f32_dpp v41, v41, v41 row_bcast:15 row_mask:0xa bank_mask:0xf
	s_nop 1
	v_max_f32_dpp v41, v41, v41 row_bcast:31 row_mask:0xc bank_mask:0xf
	s_nop 1
	v_readlane_b32 s28, v41, 63
	s_nop 1
	v_div_scale_f32 v48, s[30:31], s28, s28, v47
	v_rcp_f32_e32 v49, v48
	s_nop 0
	v_fma_f32 v50, -v48, v49, 1.0
	v_fmac_f32_e32 v49, v50, v49
	v_mov_b32_e32 v50, s28
	v_div_scale_f32 v50, vcc, s32, v50, s32
	v_mul_f32_e32 v51, v50, v49
	v_fma_f32 v52, -v48, v51, v50
	v_fmac_f32_e32 v51, v52, v49
	v_fma_f32 v48, -v48, v51, v50
	v_div_fmas_f32 v48, v48, v49, v51
	v_div_fixup_f32 v48, v48, s28, v47
	v_cmp_gt_f32_e64 vcc, s28, 0
	v_writelane_b32 v40, s28, 12
	s_nop 0
	v_cndmask_b32_e32 v48, 0, v48, vcc
	v_fmaak_f32 v49, v18, v48, 0x4b400000
	v_fmaak_f32 v50, v19, v48, 0x4b400000
	v_fmaak_f32 v51, v20, v48, 0x4b400000
	v_fmaak_f32 v52, v21, v48, 0x4b400000
	v_perm_b32 v49, v50, v49, s33
	v_perm_b32 v51, v52, v51, s34
	v_or_b32_e32 v104, v49, v51
	v_fmaak_f32 v41, v22, v48, 0x4b400000
	v_fmaak_f32 v42, v23, v48, 0x4b400000
	v_fmaak_f32 v43, v24, v48, 0x4b400000
	v_fmaak_f32 v44, v25, v48, 0x4b400000
	v_perm_b32 v41, v42, v41, s33
	v_perm_b32 v43, v44, v43, s34
	v_or_b32_e32 v105, v41, v43
	v_fmaak_f32 v49, v26, v48, 0x4b400000
	v_fmaak_f32 v50, v27, v48, 0x4b400000
	v_fmaak_f32 v51, v28, v48, 0x4b400000
	v_fmaak_f32 v52, v29, v48, 0x4b400000
	v_perm_b32 v49, v50, v49, s33
	v_perm_b32 v51, v52, v51, s34
	v_or_b32_e32 v106, v49, v51
	v_fmaak_f32 v41, v30, v48, 0x4b400000
	v_fmaak_f32 v42, v31, v48, 0x4b400000
	v_fmaak_f32 v43, v32, v48, 0x4b400000
	v_fmaak_f32 v44, v33, v48, 0x4b400000
	v_perm_b32 v41, v42, v41, s33
	v_perm_b32 v43, v44, v43, s34
	v_or_b32_e32 v107, v41, v43
	s_waitcnt vmcnt(0)
	ds_read_b128 v[18:21], v38 offset:4096
	ds_read_b128 v[22:25], v38 offset:5120
	ds_read_b128 v[26:29], v38 offset:6144
	ds_read_b128 v[30:33], v38 offset:7168
	s_waitcnt lgkmcnt(0)
	s_barrier
	s_mov_b32 m0, s35
	s_nop 0
	global_load_lds_dwordx4 v34, s[16:17] nt
	global_load_lds_dwordx4 v34, s[16:17] offset:1024 nt
	global_load_lds_dwordx4 v34, s[16:17] offset:2048 nt
	global_load_lds_dwordx4 v35, s[16:17] offset:3072 nt
	s_add_u32 s16, s16, 0x7d00
	s_addc_u32 s17, s17, 0
	v_cndmask_b32_e64 v30, 0, v30, s[18:19]
	v_cndmask_b32_e64 v31, 0, v31, s[18:19]
	v_cndmask_b32_e64 v32, 0, v32, s[18:19]
	v_cndmask_b32_e64 v33, 0, v33, s[18:19]
	v_max3_f32 v41, |v18|, |v19|, |v20|
	v_max3_f32 v42, |v21|, |v22|, |v23|
	v_max3_f32 v43, |v24|, |v25|, |v26|
	v_max3_f32 v44, |v27|, |v28|, |v29|
	v_max3_f32 v48, |v30|, |v31|, |v32|
	v_max3_f32 v41, v41, v42, |v33|
	v_max3_f32 v43, v43, v44, v48
	v_max_f32_e32 v41, v41, v43
	v_pk_add_f32 v[2:3], v[2:3], v[18:19]
	v_pk_add_f32 v[4:5], v[4:5], v[20:21]
	v_max_f32_dpp v41, v41, v41 quad_perm:[1,0,3,2] row_mask:0xf bank_mask:0xf
	v_pk_add_f32 v[6:7], v[6:7], v[22:23]
	v_pk_add_f32 v[8:9], v[8:9], v[24:25]
	v_max_f32_dpp v41, v41, v41 quad_perm:[2,3,0,1] row_mask:0xf bank_mask:0xf
	v_pk_add_f32 v[10:11], v[10:11], v[26:27]
	v_pk_add_f32 v[12:13], v[12:13], v[28:29]
	v_max_f32_dpp v41, v41, v41 row_half_mirror row_mask:0xf bank_mask:0xf
	v_pk_add_f32 v[14:15], v[14:15], v[30:31]
	v_pk_add_f32 v[16:17], v[16:17], v[32:33]
	v_max_f32_dpp v41, v41, v41 row_mirror row_mask:0xf bank_mask:0xf
	s_nop 1
	v_max_f32_dpp v41, v41, v41 row_bcast:15 row_mask:0xa bank_mask:0xf
	s_nop 1
	v_max_f32_dpp v41, v41, v41 row_bcast:31 row_mask:0xc bank_mask:0xf
	s_nop 1
	v_readlane_b32 s28, v41, 63
	s_nop 1
	v_div_scale_f32 v48, s[30:31], s28, s28, v47
	v_rcp_f32_e32 v49, v48
	s_nop 0
	v_fma_f32 v50, -v48, v49, 1.0
	v_fmac_f32_e32 v49, v50, v49
	v_mov_b32_e32 v50, s28
	v_div_scale_f32 v50, vcc, s32, v50, s32
	v_mul_f32_e32 v51, v50, v49
	v_fma_f32 v52, -v48, v51, v50
	v_fmac_f32_e32 v51, v52, v49
	v_fma_f32 v48, -v48, v51, v50
	v_div_fmas_f32 v48, v48, v49, v51
	v_div_fixup_f32 v48, v48, s28, v47
	v_cmp_gt_f32_e64 vcc, s28, 0
	v_writelane_b32 v40, s28, 13
	s_nop 0
	v_cndmask_b32_e32 v48, 0, v48, vcc
	v_fmaak_f32 v49, v18, v48, 0x4b400000
	v_fmaak_f32 v50, v19, v48, 0x4b400000
	v_fmaak_f32 v51, v20, v48, 0x4b400000
	v_fmaak_f32 v52, v21, v48, 0x4b400000
	v_perm_b32 v49, v50, v49, s33
	v_perm_b32 v51, v52, v51, s34
	v_or_b32_e32 v108, v49, v51
	v_fmaak_f32 v41, v22, v48, 0x4b400000
	v_fmaak_f32 v42, v23, v48, 0x4b400000
	v_fmaak_f32 v43, v24, v48, 0x4b400000
	v_fmaak_f32 v44, v25, v48, 0x4b400000
	v_perm_b32 v41, v42, v41, s33
	v_perm_b32 v43, v44, v43, s34
	v_or_b32_e32 v109, v41, v43
	v_fmaak_f32 v49, v26, v48, 0x4b400000
	v_fmaak_f32 v50, v27, v48, 0x4b400000
	v_fmaak_f32 v51, v28, v48, 0x4b400000
	v_fmaak_f32 v52, v29, v48, 0x4b400000
	v_perm_b32 v49, v50, v49, s33
	v_perm_b32 v51, v52, v51, s34
	v_or_b32_e32 v110, v49, v51
	v_fmaak_f32 v41, v30, v48, 0x4b400000
	v_fmaak_f32 v42, v31, v48, 0x4b400000
	v_fmaak_f32 v43, v32, v48, 0x4b400000
	v_fmaak_f32 v44, v33, v48, 0x4b400000
	v_perm_b32 v41, v42, v41, s33
	v_perm_b32 v43, v44, v43, s34
	v_or_b32_e32 v111, v41, v43
	s_waitcnt vmcnt(0)
	ds_read_b128 v[18:21], v38 offset:0
	ds_read_b128 v[22:25], v38 offset:1024
	ds_read_b128 v[26:29], v38 offset:2048
	ds_read_b128 v[30:33], v38 offset:3072
	s_waitcnt lgkmcnt(0)
	s_barrier
	s_mov_b32 m0, s36
	s_nop 0
	global_load_lds_dwordx4 v34, s[16:17] nt
	global_load_lds_dwordx4 v34, s[16:17] offset:1024 nt
	global_load_lds_dwordx4 v34, s[16:17] offset:2048 nt
	global_load_lds_dwordx4 v35, s[16:17] offset:3072 nt
	s_add_u32 s16, s16, 0x7d00
	s_addc_u32 s17, s17, 0
	v_cndmask_b32_e64 v30, 0, v30, s[18:19]
	v_cndmask_b32_e64 v31, 0, v31, s[18:19]
	v_cndmask_b32_e64 v32, 0, v32, s[18:19]
	v_cndmask_b32_e64 v33, 0, v33, s[18:19]
	v_max3_f32 v41, |v18|, |v19|, |v20|
	v_max3_f32 v42, |v21|, |v22|, |v23|
	v_max3_f32 v43, |v24|, |v25|, |v26|
	v_max3_f32 v44, |v27|, |v28|, |v29|
	v_max3_f32 v48, |v30|, |v31|, |v32|
	v_max3_f32 v41, v41, v42, |v33|
	v_max3_f32 v43, v43, v44, v48
	v_max_f32_e32 v41, v41, v43
	v_pk_add_f32 v[2:3], v[2:3], v[18:19]
	v_pk_add_f32 v[4:5], v[4:5], v[20:21]
	v_max_f32_dpp v41, v41, v41 quad_perm:[1,0,3,2] row_mask:0xf bank_mask:0xf
	v_pk_add_f32 v[6:7], v[6:7], v[22:23]
	v_pk_add_f32 v[8:9], v[8:9], v[24:25]
	v_max_f32_dpp v41, v41, v41 quad_perm:[2,3,0,1] row_mask:0xf bank_mask:0xf
	v_pk_add_f32 v[10:11], v[10:11], v[26:27]
	v_pk_add_f32 v[12:13], v[12:13], v[28:29]
	v_max_f32_dpp v41, v41, v41 row_half_mirror row_mask:0xf bank_mask:0xf
	v_pk_add_f32 v[14:15], v[14:15], v[30:31]
	v_pk_add_f32 v[16:17], v[16:17], v[32:33]
	v_max_f32_dpp v41, v41, v41 row_mirror row_mask:0xf bank_mask:0xf
	s_nop 1
	v_max_f32_dpp v41, v41, v41 row_bcast:15 row_mask:0xa bank_mask:0xf
	s_nop 1
	v_max_f32_dpp v41, v41, v41 row_bcast:31 row_mask:0xc bank_mask:0xf
	s_nop 1
	v_readlane_b32 s28, v41, 63
	s_nop 1
	v_div_scale_f32 v48, s[30:31], s28, s28, v47
	v_rcp_f32_e32 v49, v48
	s_nop 0
	v_fma_f32 v50, -v48, v49, 1.0
	v_fmac_f32_e32 v49, v50, v49
	v_mov_b32_e32 v50, s28
	v_div_scale_f32 v50, vcc, s32, v50, s32
	v_mul_f32_e32 v51, v50, v49
	v_fma_f32 v52, -v48, v51, v50
	v_fmac_f32_e32 v51, v52, v49
	v_fma_f32 v48, -v48, v51, v50
	v_div_fmas_f32 v48, v48, v49, v51
	v_div_fixup_f32 v48, v48, s28, v47
	v_cmp_gt_f32_e64 vcc, s28, 0
	v_writelane_b32 v40, s28, 14
	s_nop 0
	v_cndmask_b32_e32 v48, 0, v48, vcc
	v_fmaak_f32 v49, v18, v48, 0x4b400000
	v_fmaak_f32 v50, v19, v48, 0x4b400000
	v_fmaak_f32 v51, v20, v48, 0x4b400000
	v_fmaak_f32 v52, v21, v48, 0x4b400000
	v_perm_b32 v49, v50, v49, s33
	v_perm_b32 v51, v52, v51, s34
	v_or_b32_e32 v112, v49, v51
	v_fmaak_f32 v41, v22, v48, 0x4b400000
	v_fmaak_f32 v42, v23, v48, 0x4b400000
	v_fmaak_f32 v43, v24, v48, 0x4b400000
	v_fmaak_f32 v44, v25, v48, 0x4b400000
	v_perm_b32 v41, v42, v41, s33
	v_perm_b32 v43, v44, v43, s34
	v_or_b32_e32 v113, v41, v43
	v_fmaak_f32 v49, v26, v48, 0x4b400000
	v_fmaak_f32 v50, v27, v48, 0x4b400000
	v_fmaak_f32 v51, v28, v48, 0x4b400000
	v_fmaak_f32 v52, v29, v48, 0x4b400000
	v_perm_b32 v49, v50, v49, s33
	v_perm_b32 v51, v52, v51, s34
	v_or_b32_e32 v114, v49, v51
	v_fmaak_f32 v41, v30, v48, 0x4b400000
	v_fmaak_f32 v42, v31, v48, 0x4b400000
	v_fmaak_f32 v43, v32, v48, 0x4b400000
	v_fmaak_f32 v44, v33, v48, 0x4b400000
	v_perm_b32 v41, v42, v41, s33
	v_perm_b32 v43, v44, v43, s34
	v_or_b32_e32 v115, v41, v43
	s_waitcnt vmcnt(0)
	ds_read_b128 v[18:21], v38 offset:4096
	ds_read_b128 v[22:25], v38 offset:5120
	ds_read_b128 v[26:29], v38 offset:6144
	ds_read_b128 v[30:33], v38 offset:7168
	s_waitcnt lgkmcnt(0)
	s_barrier
	s_mov_b32 m0, s35
	s_nop 0
	global_load_lds_dwordx4 v34, s[16:17] nt
	global_load_lds_dwordx4 v34, s[16:17] offset:1024 nt
	global_load_lds_dwordx4 v34, s[16:17] offset:2048 nt
	global_load_lds_dwordx4 v35, s[16:17] offset:3072 nt
	s_add_u32 s16, s16, 0x7d00
	s_addc_u32 s17, s17, 0
	v_cndmask_b32_e64 v30, 0, v30, s[18:19]
	v_cndmask_b32_e64 v31, 0, v31, s[18:19]
	v_cndmask_b32_e64 v32, 0, v32, s[18:19]
	v_cndmask_b32_e64 v33, 0, v33, s[18:19]
	v_max3_f32 v41, |v18|, |v19|, |v20|
	v_max3_f32 v42, |v21|, |v22|, |v23|
	v_max3_f32 v43, |v24|, |v25|, |v26|
	v_max3_f32 v44, |v27|, |v28|, |v29|
	v_max3_f32 v48, |v30|, |v31|, |v32|
	v_max3_f32 v41, v41, v42, |v33|
	v_max3_f32 v43, v43, v44, v48
	v_max_f32_e32 v41, v41, v43
	v_pk_add_f32 v[2:3], v[2:3], v[18:19]
	v_pk_add_f32 v[4:5], v[4:5], v[20:21]
	v_max_f32_dpp v41, v41, v41 quad_perm:[1,0,3,2] row_mask:0xf bank_mask:0xf
	v_pk_add_f32 v[6:7], v[6:7], v[22:23]
	v_pk_add_f32 v[8:9], v[8:9], v[24:25]
	v_max_f32_dpp v41, v41, v41 quad_perm:[2,3,0,1] row_mask:0xf bank_mask:0xf
	v_pk_add_f32 v[10:11], v[10:11], v[26:27]
	v_pk_add_f32 v[12:13], v[12:13], v[28:29]
	v_max_f32_dpp v41, v41, v41 row_half_mirror row_mask:0xf bank_mask:0xf
	v_pk_add_f32 v[14:15], v[14:15], v[30:31]
	v_pk_add_f32 v[16:17], v[16:17], v[32:33]
	v_max_f32_dpp v41, v41, v41 row_mirror row_mask:0xf bank_mask:0xf
	s_nop 1
	v_max_f32_dpp v41, v41, v41 row_bcast:15 row_mask:0xa bank_mask:0xf
	s_nop 1
	v_max_f32_dpp v41, v41, v41 row_bcast:31 row_mask:0xc bank_mask:0xf
	s_nop 1
	v_readlane_b32 s28, v41, 63
	s_nop 1
	v_div_scale_f32 v48, s[30:31], s28, s28, v47
	v_rcp_f32_e32 v49, v48
	s_nop 0
	v_fma_f32 v50, -v48, v49, 1.0
	v_fmac_f32_e32 v49, v50, v49
	v_mov_b32_e32 v50, s28
	v_div_scale_f32 v50, vcc, s32, v50, s32
	v_mul_f32_e32 v51, v50, v49
	v_fma_f32 v52, -v48, v51, v50
	v_fmac_f32_e32 v51, v52, v49
	v_fma_f32 v48, -v48, v51, v50
	v_div_fmas_f32 v48, v48, v49, v51
	v_div_fixup_f32 v48, v48, s28, v47
	v_cmp_gt_f32_e64 vcc, s28, 0
	v_writelane_b32 v40, s28, 15
	s_nop 0
	v_cndmask_b32_e32 v48, 0, v48, vcc
	v_fmaak_f32 v49, v18, v48, 0x4b400000
	v_fmaak_f32 v50, v19, v48, 0x4b400000
	v_fmaak_f32 v51, v20, v48, 0x4b400000
	v_fmaak_f32 v52, v21, v48, 0x4b400000
	v_perm_b32 v49, v50, v49, s33
	v_perm_b32 v51, v52, v51, s34
	v_or_b32_e32 v116, v49, v51
	v_fmaak_f32 v41, v22, v48, 0x4b400000
	v_fmaak_f32 v42, v23, v48, 0x4b400000
	v_fmaak_f32 v43, v24, v48, 0x4b400000
	v_fmaak_f32 v44, v25, v48, 0x4b400000
	v_perm_b32 v41, v42, v41, s33
	v_perm_b32 v43, v44, v43, s34
	v_or_b32_e32 v117, v41, v43
	v_fmaak_f32 v49, v26, v48, 0x4b400000
	v_fmaak_f32 v50, v27, v48, 0x4b400000
	v_fmaak_f32 v51, v28, v48, 0x4b400000
	v_fmaak_f32 v52, v29, v48, 0x4b400000
	v_perm_b32 v49, v50, v49, s33
	v_perm_b32 v51, v52, v51, s34
	v_or_b32_e32 v118, v49, v51
	v_fmaak_f32 v41, v30, v48, 0x4b400000
	v_fmaak_f32 v42, v31, v48, 0x4b400000
	v_fmaak_f32 v43, v32, v48, 0x4b400000
	v_fmaak_f32 v44, v33, v48, 0x4b400000
	v_perm_b32 v41, v42, v41, s33
	v_perm_b32 v43, v44, v43, s34
	v_or_b32_e32 v119, v41, v43
	s_waitcnt vmcnt(0)
	ds_read_b128 v[18:21], v38 offset:0
	ds_read_b128 v[22:25], v38 offset:1024
	ds_read_b128 v[26:29], v38 offset:2048
	ds_read_b128 v[30:33], v38 offset:3072
	s_waitcnt lgkmcnt(0)
	s_barrier
	s_mov_b32 m0, s36
	s_nop 0
	global_load_lds_dwordx4 v34, s[16:17] nt
	global_load_lds_dwordx4 v34, s[16:17] offset:1024 nt
	global_load_lds_dwordx4 v34, s[16:17] offset:2048 nt
	global_load_lds_dwordx4 v35, s[16:17] offset:3072 nt
	s_add_u32 s16, s16, 0x7d00
	s_addc_u32 s17, s17, 0
	v_cndmask_b32_e64 v30, 0, v30, s[18:19]
	v_cndmask_b32_e64 v31, 0, v31, s[18:19]
	v_cndmask_b32_e64 v32, 0, v32, s[18:19]
	v_cndmask_b32_e64 v33, 0, v33, s[18:19]
	v_max3_f32 v41, |v18|, |v19|, |v20|
	v_max3_f32 v42, |v21|, |v22|, |v23|
	v_max3_f32 v43, |v24|, |v25|, |v26|
	v_max3_f32 v44, |v27|, |v28|, |v29|
	v_max3_f32 v48, |v30|, |v31|, |v32|
	v_max3_f32 v41, v41, v42, |v33|
	v_max3_f32 v43, v43, v44, v48
	v_max_f32_e32 v41, v41, v43
	v_pk_add_f32 v[2:3], v[2:3], v[18:19]
	v_pk_add_f32 v[4:5], v[4:5], v[20:21]
	v_max_f32_dpp v41, v41, v41 quad_perm:[1,0,3,2] row_mask:0xf bank_mask:0xf
	v_pk_add_f32 v[6:7], v[6:7], v[22:23]
	v_pk_add_f32 v[8:9], v[8:9], v[24:25]
	v_max_f32_dpp v41, v41, v41 quad_perm:[2,3,0,1] row_mask:0xf bank_mask:0xf
	v_pk_add_f32 v[10:11], v[10:11], v[26:27]
	v_pk_add_f32 v[12:13], v[12:13], v[28:29]
	v_max_f32_dpp v41, v41, v41 row_half_mirror row_mask:0xf bank_mask:0xf
	v_pk_add_f32 v[14:15], v[14:15], v[30:31]
	v_pk_add_f32 v[16:17], v[16:17], v[32:33]
	v_max_f32_dpp v41, v41, v41 row_mirror row_mask:0xf bank_mask:0xf
	s_nop 1
	v_max_f32_dpp v41, v41, v41 row_bcast:15 row_mask:0xa bank_mask:0xf
	s_nop 1
	v_max_f32_dpp v41, v41, v41 row_bcast:31 row_mask:0xc bank_mask:0xf
	s_nop 1
	v_readlane_b32 s28, v41, 63
	s_nop 1
	v_div_scale_f32 v48, s[30:31], s28, s28, v47
	v_rcp_f32_e32 v49, v48
	s_nop 0
	v_fma_f32 v50, -v48, v49, 1.0
	v_fmac_f32_e32 v49, v50, v49
	v_mov_b32_e32 v50, s28
	v_div_scale_f32 v50, vcc, s32, v50, s32
	v_mul_f32_e32 v51, v50, v49
	v_fma_f32 v52, -v48, v51, v50
	v_fmac_f32_e32 v51, v52, v49
	v_fma_f32 v48, -v48, v51, v50
	v_div_fmas_f32 v48, v48, v49, v51
	v_div_fixup_f32 v48, v48, s28, v47
	v_cmp_gt_f32_e64 vcc, s28, 0
	v_writelane_b32 v40, s28, 16
	s_nop 0
	v_cndmask_b32_e32 v48, 0, v48, vcc
	v_fmaak_f32 v49, v18, v48, 0x4b400000
	v_fmaak_f32 v50, v19, v48, 0x4b400000
	v_fmaak_f32 v51, v20, v48, 0x4b400000
	v_fmaak_f32 v52, v21, v48, 0x4b400000
	v_perm_b32 v49, v50, v49, s33
	v_perm_b32 v51, v52, v51, s34
	v_or_b32_e32 v120, v49, v51
	v_fmaak_f32 v41, v22, v48, 0x4b400000
	v_fmaak_f32 v42, v23, v48, 0x4b400000
	v_fmaak_f32 v43, v24, v48, 0x4b400000
	v_fmaak_f32 v44, v25, v48, 0x4b400000
	v_perm_b32 v41, v42, v41, s33
	v_perm_b32 v43, v44, v43, s34
	v_or_b32_e32 v121, v41, v43
	v_fmaak_f32 v49, v26, v48, 0x4b400000
	v_fmaak_f32 v50, v27, v48, 0x4b400000
	v_fmaak_f32 v51, v28, v48, 0x4b400000
	v_fmaak_f32 v52, v29, v48, 0x4b400000
	v_perm_b32 v49, v50, v49, s33
	v_perm_b32 v51, v52, v51, s34
	v_or_b32_e32 v122, v49, v51
	v_fmaak_f32 v41, v30, v48, 0x4b400000
	v_fmaak_f32 v42, v31, v48, 0x4b400000
	v_fmaak_f32 v43, v32, v48, 0x4b400000
	v_fmaak_f32 v44, v33, v48, 0x4b400000
	v_perm_b32 v41, v42, v41, s33
	v_perm_b32 v43, v44, v43, s34
	v_or_b32_e32 v123, v41, v43
	s_waitcnt vmcnt(0)
	ds_read_b128 v[18:21], v38 offset:4096
	ds_read_b128 v[22:25], v38 offset:5120
	ds_read_b128 v[26:29], v38 offset:6144
	ds_read_b128 v[30:33], v38 offset:7168
	s_waitcnt lgkmcnt(0)
	s_barrier
	s_mov_b32 m0, s35
	s_nop 0
	global_load_lds_dwordx4 v34, s[16:17] nt
	global_load_lds_dwordx4 v34, s[16:17] offset:1024 nt
	global_load_lds_dwordx4 v34, s[16:17] offset:2048 nt
	global_load_lds_dwordx4 v35, s[16:17] offset:3072 nt
	s_add_u32 s16, s16, 0x7d00
	s_addc_u32 s17, s17, 0
	v_cndmask_b32_e64 v30, 0, v30, s[18:19]
	v_cndmask_b32_e64 v31, 0, v31, s[18:19]
	v_cndmask_b32_e64 v32, 0, v32, s[18:19]
	v_cndmask_b32_e64 v33, 0, v33, s[18:19]
	v_max3_f32 v41, |v18|, |v19|, |v20|
	v_max3_f32 v42, |v21|, |v22|, |v23|
	v_max3_f32 v43, |v24|, |v25|, |v26|
	v_max3_f32 v44, |v27|, |v28|, |v29|
	v_max3_f32 v48, |v30|, |v31|, |v32|
	v_max3_f32 v41, v41, v42, |v33|
	v_max3_f32 v43, v43, v44, v48
	v_max_f32_e32 v41, v41, v43
	v_pk_add_f32 v[2:3], v[2:3], v[18:19]
	v_pk_add_f32 v[4:5], v[4:5], v[20:21]
	v_max_f32_dpp v41, v41, v41 quad_perm:[1,0,3,2] row_mask:0xf bank_mask:0xf
	v_pk_add_f32 v[6:7], v[6:7], v[22:23]
	v_pk_add_f32 v[8:9], v[8:9], v[24:25]
	v_max_f32_dpp v41, v41, v41 quad_perm:[2,3,0,1] row_mask:0xf bank_mask:0xf
	v_pk_add_f32 v[10:11], v[10:11], v[26:27]
	v_pk_add_f32 v[12:13], v[12:13], v[28:29]
	v_max_f32_dpp v41, v41, v41 row_half_mirror row_mask:0xf bank_mask:0xf
	v_pk_add_f32 v[14:15], v[14:15], v[30:31]
	v_pk_add_f32 v[16:17], v[16:17], v[32:33]
	v_max_f32_dpp v41, v41, v41 row_mirror row_mask:0xf bank_mask:0xf
	s_nop 1
	v_max_f32_dpp v41, v41, v41 row_bcast:15 row_mask:0xa bank_mask:0xf
	s_nop 1
	v_max_f32_dpp v41, v41, v41 row_bcast:31 row_mask:0xc bank_mask:0xf
	s_nop 1
	v_readlane_b32 s28, v41, 63
	s_nop 1
	v_div_scale_f32 v48, s[30:31], s28, s28, v47
	v_rcp_f32_e32 v49, v48
	s_nop 0
	v_fma_f32 v50, -v48, v49, 1.0
	v_fmac_f32_e32 v49, v50, v49
	v_mov_b32_e32 v50, s28
	v_div_scale_f32 v50, vcc, s32, v50, s32
	v_mul_f32_e32 v51, v50, v49
	v_fma_f32 v52, -v48, v51, v50
	v_fmac_f32_e32 v51, v52, v49
	v_fma_f32 v48, -v48, v51, v50
	v_div_fmas_f32 v48, v48, v49, v51
	v_div_fixup_f32 v48, v48, s28, v47
	v_cmp_gt_f32_e64 vcc, s28, 0
	v_writelane_b32 v40, s28, 17
	s_nop 0
	v_cndmask_b32_e32 v48, 0, v48, vcc
	v_fmaak_f32 v49, v18, v48, 0x4b400000
	v_fmaak_f32 v50, v19, v48, 0x4b400000
	v_fmaak_f32 v51, v20, v48, 0x4b400000
	v_fmaak_f32 v52, v21, v48, 0x4b400000
	v_perm_b32 v49, v50, v49, s33
	v_perm_b32 v51, v52, v51, s34
	v_or_b32_e32 v124, v49, v51
	v_fmaak_f32 v41, v22, v48, 0x4b400000
	v_fmaak_f32 v42, v23, v48, 0x4b400000
	v_fmaak_f32 v43, v24, v48, 0x4b400000
	v_fmaak_f32 v44, v25, v48, 0x4b400000
	v_perm_b32 v41, v42, v41, s33
	v_perm_b32 v43, v44, v43, s34
	v_or_b32_e32 v125, v41, v43
	v_fmaak_f32 v49, v26, v48, 0x4b400000
	v_fmaak_f32 v50, v27, v48, 0x4b400000
	v_fmaak_f32 v51, v28, v48, 0x4b400000
	v_fmaak_f32 v52, v29, v48, 0x4b400000
	v_perm_b32 v49, v50, v49, s33
	v_perm_b32 v51, v52, v51, s34
	v_or_b32_e32 v126, v49, v51
	v_fmaak_f32 v41, v30, v48, 0x4b400000
	v_fmaak_f32 v42, v31, v48, 0x4b400000
	v_fmaak_f32 v43, v32, v48, 0x4b400000
	v_fmaak_f32 v44, v33, v48, 0x4b400000
	v_perm_b32 v41, v42, v41, s33
	v_perm_b32 v43, v44, v43, s34
	v_or_b32_e32 v127, v41, v43
	s_waitcnt vmcnt(0)
	ds_read_b128 v[18:21], v38 offset:0
	ds_read_b128 v[22:25], v38 offset:1024
	ds_read_b128 v[26:29], v38 offset:2048
	ds_read_b128 v[30:33], v38 offset:3072
	s_waitcnt lgkmcnt(0)
	s_barrier
	s_mov_b32 m0, s36
	s_nop 0
	global_load_lds_dwordx4 v34, s[16:17] nt
	global_load_lds_dwordx4 v34, s[16:17] offset:1024 nt
	global_load_lds_dwordx4 v34, s[16:17] offset:2048 nt
	global_load_lds_dwordx4 v35, s[16:17] offset:3072 nt
	s_add_u32 s16, s16, 0x7d00
	s_addc_u32 s17, s17, 0
	v_cndmask_b32_e64 v30, 0, v30, s[18:19]
	v_cndmask_b32_e64 v31, 0, v31, s[18:19]
	v_cndmask_b32_e64 v32, 0, v32, s[18:19]
	v_cndmask_b32_e64 v33, 0, v33, s[18:19]
	v_max3_f32 v41, |v18|, |v19|, |v20|
	v_max3_f32 v42, |v21|, |v22|, |v23|
	v_max3_f32 v43, |v24|, |v25|, |v26|
	v_max3_f32 v44, |v27|, |v28|, |v29|
	v_max3_f32 v48, |v30|, |v31|, |v32|
	v_max3_f32 v41, v41, v42, |v33|
	v_max3_f32 v43, v43, v44, v48
	v_max_f32_e32 v41, v41, v43
	v_pk_add_f32 v[2:3], v[2:3], v[18:19]
	v_pk_add_f32 v[4:5], v[4:5], v[20:21]
	v_max_f32_dpp v41, v41, v41 quad_perm:[1,0,3,2] row_mask:0xf bank_mask:0xf
	v_pk_add_f32 v[6:7], v[6:7], v[22:23]
	v_pk_add_f32 v[8:9], v[8:9], v[24:25]
	v_max_f32_dpp v41, v41, v41 quad_perm:[2,3,0,1] row_mask:0xf bank_mask:0xf
	v_pk_add_f32 v[10:11], v[10:11], v[26:27]
	v_pk_add_f32 v[12:13], v[12:13], v[28:29]
	v_max_f32_dpp v41, v41, v41 row_half_mirror row_mask:0xf bank_mask:0xf
	v_pk_add_f32 v[14:15], v[14:15], v[30:31]
	v_pk_add_f32 v[16:17], v[16:17], v[32:33]
	v_max_f32_dpp v41, v41, v41 row_mirror row_mask:0xf bank_mask:0xf
	s_nop 1
	v_max_f32_dpp v41, v41, v41 row_bcast:15 row_mask:0xa bank_mask:0xf
	s_nop 1
	v_max_f32_dpp v41, v41, v41 row_bcast:31 row_mask:0xc bank_mask:0xf
	s_nop 1
	v_readlane_b32 s28, v41, 63
	s_nop 1
	v_div_scale_f32 v48, s[30:31], s28, s28, v47
	v_rcp_f32_e32 v49, v48
	s_nop 0
	v_fma_f32 v50, -v48, v49, 1.0
	v_fmac_f32_e32 v49, v50, v49
	v_mov_b32_e32 v50, s28
	v_div_scale_f32 v50, vcc, s32, v50, s32
	v_mul_f32_e32 v51, v50, v49
	v_fma_f32 v52, -v48, v51, v50
	v_fmac_f32_e32 v51, v52, v49
	v_fma_f32 v48, -v48, v51, v50
	v_div_fmas_f32 v48, v48, v49, v51
	v_div_fixup_f32 v48, v48, s28, v47
	v_cmp_gt_f32_e64 vcc, s28, 0
	v_writelane_b32 v40, s28, 18
	s_nop 0
	v_cndmask_b32_e32 v48, 0, v48, vcc
	v_fmaak_f32 v49, v18, v48, 0x4b400000
	v_fmaak_f32 v50, v19, v48, 0x4b400000
	v_fmaak_f32 v51, v20, v48, 0x4b400000
	v_fmaak_f32 v52, v21, v48, 0x4b400000
	v_perm_b32 v49, v50, v49, s33
	v_perm_b32 v51, v52, v51, s34
	v_or_b32_e32 v49, v49, v51
	s_add_u32 s20, s20, 0x4800
	s_addc_u32 s21, s21, 0
	s_add_u32 s22, s22, 0x4800
	s_addc_u32 s23, s23, 0
	s_add_u32 s24, s24, 0x4800
	s_addc_u32 s25, s25, 0
	s_add_u32 s26, s26, 0x4800
	s_addc_u32 s27, s27, 0
	global_store_dword v39, v49, s[20:21]
	v_fmaak_f32 v41, v22, v48, 0x4b400000
	v_fmaak_f32 v42, v23, v48, 0x4b400000
	v_fmaak_f32 v43, v24, v48, 0x4b400000
	v_fmaak_f32 v44, v25, v48, 0x4b400000
	v_perm_b32 v41, v42, v41, s33
	v_perm_b32 v43, v44, v43, s34
	v_or_b32_e32 v41, v41, v43
	global_store_dword v39, v41, s[22:23]
	v_fmaak_f32 v49, v26, v48, 0x4b400000
	v_fmaak_f32 v50, v27, v48, 0x4b400000
	v_fmaak_f32 v51, v28, v48, 0x4b400000
	v_fmaak_f32 v52, v29, v48, 0x4b400000
	v_perm_b32 v49, v50, v49, s33
	v_perm_b32 v51, v52, v51, s34
	v_or_b32_e32 v49, v49, v51
	global_store_dword v39, v49, s[24:25]
	v_fmaak_f32 v41, v30, v48, 0x4b400000
	v_fmaak_f32 v42, v31, v48, 0x4b400000
	v_fmaak_f32 v43, v32, v48, 0x4b400000
	v_fmaak_f32 v44, v33, v48, 0x4b400000
	v_perm_b32 v41, v42, v41, s33
	v_perm_b32 v43, v44, v43, s34
	v_or_b32_e32 v41, v41, v43
	global_store_dword v39, v41, s[26:27]
	s_waitcnt vmcnt(4)
	ds_read_b128 v[18:21], v38 offset:4096
	ds_read_b128 v[22:25], v38 offset:5120
	ds_read_b128 v[26:29], v38 offset:6144
	ds_read_b128 v[30:33], v38 offset:7168
	s_waitcnt lgkmcnt(0)
	s_barrier
	s_mov_b32 m0, s35
	s_nop 0
	global_load_lds_dwordx4 v34, s[16:17] nt
	global_load_lds_dwordx4 v34, s[16:17] offset:1024 nt
	global_load_lds_dwordx4 v34, s[16:17] offset:2048 nt
	global_load_lds_dwordx4 v35, s[16:17] offset:3072 nt
	s_add_u32 s16, s16, 0x7d00
	s_addc_u32 s17, s17, 0
	v_cndmask_b32_e64 v30, 0, v30, s[18:19]
	v_cndmask_b32_e64 v31, 0, v31, s[18:19]
	v_cndmask_b32_e64 v32, 0, v32, s[18:19]
	v_cndmask_b32_e64 v33, 0, v33, s[18:19]
	v_max3_f32 v41, |v18|, |v19|, |v20|
	v_max3_f32 v42, |v21|, |v22|, |v23|
	v_max3_f32 v43, |v24|, |v25|, |v26|
	v_max3_f32 v44, |v27|, |v28|, |v29|
	v_max3_f32 v48, |v30|, |v31|, |v32|
	v_max3_f32 v41, v41, v42, |v33|
	v_max3_f32 v43, v43, v44, v48
	v_max_f32_e32 v41, v41, v43
	v_pk_add_f32 v[2:3], v[2:3], v[18:19]
	v_pk_add_f32 v[4:5], v[4:5], v[20:21]
	v_max_f32_dpp v41, v41, v41 quad_perm:[1,0,3,2] row_mask:0xf bank_mask:0xf
	v_pk_add_f32 v[6:7], v[6:7], v[22:23]
	v_pk_add_f32 v[8:9], v[8:9], v[24:25]
	v_max_f32_dpp v41, v41, v41 quad_perm:[2,3,0,1] row_mask:0xf bank_mask:0xf
	v_pk_add_f32 v[10:11], v[10:11], v[26:27]
	v_pk_add_f32 v[12:13], v[12:13], v[28:29]
	v_max_f32_dpp v41, v41, v41 row_half_mirror row_mask:0xf bank_mask:0xf
	v_pk_add_f32 v[14:15], v[14:15], v[30:31]
	v_pk_add_f32 v[16:17], v[16:17], v[32:33]
	v_max_f32_dpp v41, v41, v41 row_mirror row_mask:0xf bank_mask:0xf
	s_nop 1
	v_max_f32_dpp v41, v41, v41 row_bcast:15 row_mask:0xa bank_mask:0xf
	s_nop 1
	v_max_f32_dpp v41, v41, v41 row_bcast:31 row_mask:0xc bank_mask:0xf
	s_nop 1
	v_readlane_b32 s28, v41, 63
	s_nop 1
	v_div_scale_f32 v48, s[30:31], s28, s28, v47
	v_rcp_f32_e32 v49, v48
	s_nop 0
	v_fma_f32 v50, -v48, v49, 1.0
	v_fmac_f32_e32 v49, v50, v49
	v_mov_b32_e32 v50, s28
	v_div_scale_f32 v50, vcc, s32, v50, s32
	v_mul_f32_e32 v51, v50, v49
	v_fma_f32 v52, -v48, v51, v50
	v_fmac_f32_e32 v51, v52, v49
	v_fma_f32 v48, -v48, v51, v50
	v_div_fmas_f32 v48, v48, v49, v51
	v_div_fixup_f32 v48, v48, s28, v47
	v_cmp_gt_f32_e64 vcc, s28, 0
	v_writelane_b32 v40, s28, 19
	s_nop 0
	v_cndmask_b32_e32 v48, 0, v48, vcc
	v_fmaak_f32 v49, v18, v48, 0x4b400000
	v_fmaak_f32 v50, v19, v48, 0x4b400000
	v_fmaak_f32 v51, v20, v48, 0x4b400000
	v_fmaak_f32 v52, v21, v48, 0x4b400000
	v_perm_b32 v49, v50, v49, s33
	v_perm_b32 v51, v52, v51, s34
	v_or_b32_e32 v49, v49, v51
	s_add_u32 s20, s20, 0x400
	s_addc_u32 s21, s21, 0
	s_add_u32 s22, s22, 0x400
	s_addc_u32 s23, s23, 0
	s_add_u32 s24, s24, 0x400
	s_addc_u32 s25, s25, 0
	s_add_u32 s26, s26, 0x400
	s_addc_u32 s27, s27, 0
	global_store_dword v39, v49, s[20:21]
	v_fmaak_f32 v41, v22, v48, 0x4b400000
	v_fmaak_f32 v42, v23, v48, 0x4b400000
	v_fmaak_f32 v43, v24, v48, 0x4b400000
	v_fmaak_f32 v44, v25, v48, 0x4b400000
	v_perm_b32 v41, v42, v41, s33
	v_perm_b32 v43, v44, v43, s34
	v_or_b32_e32 v41, v41, v43
	global_store_dword v39, v41, s[22:23]
	v_fmaak_f32 v49, v26, v48, 0x4b400000
	v_fmaak_f32 v50, v27, v48, 0x4b400000
	v_fmaak_f32 v51, v28, v48, 0x4b400000
	v_fmaak_f32 v52, v29, v48, 0x4b400000
	v_perm_b32 v49, v50, v49, s33
	v_perm_b32 v51, v52, v51, s34
	v_or_b32_e32 v49, v49, v51
	global_store_dword v39, v49, s[24:25]
	v_fmaak_f32 v41, v30, v48, 0x4b400000
	v_fmaak_f32 v42, v31, v48, 0x4b400000
	v_fmaak_f32 v43, v32, v48, 0x4b400000
	v_fmaak_f32 v44, v33, v48, 0x4b400000
	v_perm_b32 v41, v42, v41, s33
	v_perm_b32 v43, v44, v43, s34
	v_or_b32_e32 v41, v41, v43
	global_store_dword v39, v41, s[26:27]
	s_waitcnt vmcnt(4)
	ds_read_b128 v[18:21], v38 offset:0
	ds_read_b128 v[22:25], v38 offset:1024
	ds_read_b128 v[26:29], v38 offset:2048
	ds_read_b128 v[30:33], v38 offset:3072
	s_waitcnt lgkmcnt(0)
	s_barrier
	s_mov_b32 m0, s36
	s_nop 0
	global_load_lds_dwordx4 v34, s[16:17] nt
	global_load_lds_dwordx4 v34, s[16:17] offset:1024 nt
	global_load_lds_dwordx4 v34, s[16:17] offset:2048 nt
	global_load_lds_dwordx4 v35, s[16:17] offset:3072 nt
	s_add_u32 s16, s16, 0x7d00
	s_addc_u32 s17, s17, 0
	v_cndmask_b32_e64 v30, 0, v30, s[18:19]
	v_cndmask_b32_e64 v31, 0, v31, s[18:19]
	v_cndmask_b32_e64 v32, 0, v32, s[18:19]
	v_cndmask_b32_e64 v33, 0, v33, s[18:19]
	v_max3_f32 v41, |v18|, |v19|, |v20|
	v_max3_f32 v42, |v21|, |v22|, |v23|
	v_max3_f32 v43, |v24|, |v25|, |v26|
	v_max3_f32 v44, |v27|, |v28|, |v29|
	v_max3_f32 v48, |v30|, |v31|, |v32|
	v_max3_f32 v41, v41, v42, |v33|
	v_max3_f32 v43, v43, v44, v48
	v_max_f32_e32 v41, v41, v43
	v_pk_add_f32 v[2:3], v[2:3], v[18:19]
	v_pk_add_f32 v[4:5], v[4:5], v[20:21]
	v_max_f32_dpp v41, v41, v41 quad_perm:[1,0,3,2] row_mask:0xf bank_mask:0xf
	v_pk_add_f32 v[6:7], v[6:7], v[22:23]
	v_pk_add_f32 v[8:9], v[8:9], v[24:25]
	v_max_f32_dpp v41, v41, v41 quad_perm:[2,3,0,1] row_mask:0xf bank_mask:0xf
	v_pk_add_f32 v[10:11], v[10:11], v[26:27]
	v_pk_add_f32 v[12:13], v[12:13], v[28:29]
	v_max_f32_dpp v41, v41, v41 row_half_mirror row_mask:0xf bank_mask:0xf
	v_pk_add_f32 v[14:15], v[14:15], v[30:31]
	v_pk_add_f32 v[16:17], v[16:17], v[32:33]
	v_max_f32_dpp v41, v41, v41 row_mirror row_mask:0xf bank_mask:0xf
	s_nop 1
	v_max_f32_dpp v41, v41, v41 row_bcast:15 row_mask:0xa bank_mask:0xf
	s_nop 1
	v_max_f32_dpp v41, v41, v41 row_bcast:31 row_mask:0xc bank_mask:0xf
	s_nop 1
	v_readlane_b32 s28, v41, 63
	s_nop 1
	v_div_scale_f32 v48, s[30:31], s28, s28, v47
	v_rcp_f32_e32 v49, v48
	s_nop 0
	v_fma_f32 v50, -v48, v49, 1.0
	v_fmac_f32_e32 v49, v50, v49
	v_mov_b32_e32 v50, s28
	v_div_scale_f32 v50, vcc, s32, v50, s32
	v_mul_f32_e32 v51, v50, v49
	v_fma_f32 v52, -v48, v51, v50
	v_fmac_f32_e32 v51, v52, v49
	v_fma_f32 v48, -v48, v51, v50
	v_div_fmas_f32 v48, v48, v49, v51
	v_div_fixup_f32 v48, v48, s28, v47
	v_cmp_gt_f32_e64 vcc, s28, 0
	v_writelane_b32 v40, s28, 20
	s_nop 0
	v_cndmask_b32_e32 v48, 0, v48, vcc
	v_fmaak_f32 v49, v18, v48, 0x4b400000
	v_fmaak_f32 v50, v19, v48, 0x4b400000
	v_fmaak_f32 v51, v20, v48, 0x4b400000
	v_fmaak_f32 v52, v21, v48, 0x4b400000
	v_perm_b32 v49, v50, v49, s33
	v_perm_b32 v51, v52, v51, s34
	v_or_b32_e32 v49, v49, v51
	s_add_u32 s20, s20, 0x400
	s_addc_u32 s21, s21, 0
	s_add_u32 s22, s22, 0x400
	s_addc_u32 s23, s23, 0
	s_add_u32 s24, s24, 0x400
	s_addc_u32 s25, s25, 0
	s_add_u32 s26, s26, 0x400
	s_addc_u32 s27, s27, 0
	global_store_dword v39, v49, s[20:21]
	v_fmaak_f32 v41, v22, v48, 0x4b400000
	v_fmaak_f32 v42, v23, v48, 0x4b400000
	v_fmaak_f32 v43, v24, v48, 0x4b400000
	v_fmaak_f32 v44, v25, v48, 0x4b400000
	v_perm_b32 v41, v42, v41, s33
	v_perm_b32 v43, v44, v43, s34
	v_or_b32_e32 v41, v41, v43
	global_store_dword v39, v41, s[22:23]
	v_fmaak_f32 v49, v26, v48, 0x4b400000
	v_fmaak_f32 v50, v27, v48, 0x4b400000
	v_fmaak_f32 v51, v28, v48, 0x4b400000
	v_fmaak_f32 v52, v29, v48, 0x4b400000
	v_perm_b32 v49, v50, v49, s33
	v_perm_b32 v51, v52, v51, s34
	v_or_b32_e32 v49, v49, v51
	global_store_dword v39, v49, s[24:25]
	v_fmaak_f32 v41, v30, v48, 0x4b400000
	v_fmaak_f32 v42, v31, v48, 0x4b400000
	v_fmaak_f32 v43, v32, v48, 0x4b400000
	v_fmaak_f32 v44, v33, v48, 0x4b400000
	v_perm_b32 v41, v42, v41, s33
	v_perm_b32 v43, v44, v43, s34
	v_or_b32_e32 v41, v41, v43
	global_store_dword v39, v41, s[26:27]
	s_waitcnt vmcnt(4)
	ds_read_b128 v[18:21], v38 offset:4096
	ds_read_b128 v[22:25], v38 offset:5120
	ds_read_b128 v[26:29], v38 offset:6144
	ds_read_b128 v[30:33], v38 offset:7168
	s_waitcnt lgkmcnt(0)
	s_barrier
	s_mov_b32 m0, s35
	s_nop 0
	global_load_lds_dwordx4 v34, s[16:17] nt
	global_load_lds_dwordx4 v34, s[16:17] offset:1024 nt
	global_load_lds_dwordx4 v34, s[16:17] offset:2048 nt
	global_load_lds_dwordx4 v35, s[16:17] offset:3072 nt
	s_add_u32 s16, s16, 0x7d00
	s_addc_u32 s17, s17, 0
	v_cndmask_b32_e64 v30, 0, v30, s[18:19]
	v_cndmask_b32_e64 v31, 0, v31, s[18:19]
	v_cndmask_b32_e64 v32, 0, v32, s[18:19]
	v_cndmask_b32_e64 v33, 0, v33, s[18:19]
	v_max3_f32 v41, |v18|, |v19|, |v20|
	v_max3_f32 v42, |v21|, |v22|, |v23|
	v_max3_f32 v43, |v24|, |v25|, |v26|
	v_max3_f32 v44, |v27|, |v28|, |v29|
	v_max3_f32 v48, |v30|, |v31|, |v32|
	v_max3_f32 v41, v41, v42, |v33|
	v_max3_f32 v43, v43, v44, v48
	v_max_f32_e32 v41, v41, v43
	v_pk_add_f32 v[2:3], v[2:3], v[18:19]
	v_pk_add_f32 v[4:5], v[4:5], v[20:21]
	v_max_f32_dpp v41, v41, v41 quad_perm:[1,0,3,2] row_mask:0xf bank_mask:0xf
	v_pk_add_f32 v[6:7], v[6:7], v[22:23]
	v_pk_add_f32 v[8:9], v[8:9], v[24:25]
	v_max_f32_dpp v41, v41, v41 quad_perm:[2,3,0,1] row_mask:0xf bank_mask:0xf
	v_pk_add_f32 v[10:11], v[10:11], v[26:27]
	v_pk_add_f32 v[12:13], v[12:13], v[28:29]
	v_max_f32_dpp v41, v41, v41 row_half_mirror row_mask:0xf bank_mask:0xf
	v_pk_add_f32 v[14:15], v[14:15], v[30:31]
	v_pk_add_f32 v[16:17], v[16:17], v[32:33]
	v_max_f32_dpp v41, v41, v41 row_mirror row_mask:0xf bank_mask:0xf
	s_nop 1
	v_max_f32_dpp v41, v41, v41 row_bcast:15 row_mask:0xa bank_mask:0xf
	s_nop 1
	v_max_f32_dpp v41, v41, v41 row_bcast:31 row_mask:0xc bank_mask:0xf
	s_nop 1
	v_readlane_b32 s28, v41, 63
	s_nop 1
	v_div_scale_f32 v48, s[30:31], s28, s28, v47
	v_rcp_f32_e32 v49, v48
	s_nop 0
	v_fma_f32 v50, -v48, v49, 1.0
	v_fmac_f32_e32 v49, v50, v49
	v_mov_b32_e32 v50, s28
	v_div_scale_f32 v50, vcc, s32, v50, s32
	v_mul_f32_e32 v51, v50, v49
	v_fma_f32 v52, -v48, v51, v50
	v_fmac_f32_e32 v51, v52, v49
	v_fma_f32 v48, -v48, v51, v50
	v_div_fmas_f32 v48, v48, v49, v51
	v_div_fixup_f32 v48, v48, s28, v47
	v_cmp_gt_f32_e64 vcc, s28, 0
	v_writelane_b32 v40, s28, 21
	s_nop 0
	v_cndmask_b32_e32 v48, 0, v48, vcc
	v_fmaak_f32 v49, v18, v48, 0x4b400000
	v_fmaak_f32 v50, v19, v48, 0x4b400000
	v_fmaak_f32 v51, v20, v48, 0x4b400000
	v_fmaak_f32 v52, v21, v48, 0x4b400000
	v_perm_b32 v49, v50, v49, s33
	v_perm_b32 v51, v52, v51, s34
	v_or_b32_e32 v49, v49, v51
	s_add_u32 s20, s20, 0x400
	s_addc_u32 s21, s21, 0
	s_add_u32 s22, s22, 0x400
	s_addc_u32 s23, s23, 0
	s_add_u32 s24, s24, 0x400
	s_addc_u32 s25, s25, 0
	s_add_u32 s26, s26, 0x400
	s_addc_u32 s27, s27, 0
	global_store_dword v39, v49, s[20:21]
	v_fmaak_f32 v41, v22, v48, 0x4b400000
	v_fmaak_f32 v42, v23, v48, 0x4b400000
	v_fmaak_f32 v43, v24, v48, 0x4b400000
	v_fmaak_f32 v44, v25, v48, 0x4b400000
	v_perm_b32 v41, v42, v41, s33
	v_perm_b32 v43, v44, v43, s34
	v_or_b32_e32 v41, v41, v43
	global_store_dword v39, v41, s[22:23]
	v_fmaak_f32 v49, v26, v48, 0x4b400000
	v_fmaak_f32 v50, v27, v48, 0x4b400000
	v_fmaak_f32 v51, v28, v48, 0x4b400000
	v_fmaak_f32 v52, v29, v48, 0x4b400000
	v_perm_b32 v49, v50, v49, s33
	v_perm_b32 v51, v52, v51, s34
	v_or_b32_e32 v49, v49, v51
	global_store_dword v39, v49, s[24:25]
	v_fmaak_f32 v41, v30, v48, 0x4b400000
	v_fmaak_f32 v42, v31, v48, 0x4b400000
	v_fmaak_f32 v43, v32, v48, 0x4b400000
	v_fmaak_f32 v44, v33, v48, 0x4b400000
	v_perm_b32 v41, v42, v41, s33
	v_perm_b32 v43, v44, v43, s34
	v_or_b32_e32 v41, v41, v43
	global_store_dword v39, v41, s[26:27]
	s_waitcnt vmcnt(4)
	ds_read_b128 v[18:21], v38 offset:0
	ds_read_b128 v[22:25], v38 offset:1024
	ds_read_b128 v[26:29], v38 offset:2048
	ds_read_b128 v[30:33], v38 offset:3072
	s_waitcnt lgkmcnt(0)
	s_barrier
	s_mov_b32 m0, s36
	s_nop 0
	global_load_lds_dwordx4 v34, s[16:17] nt
	global_load_lds_dwordx4 v34, s[16:17] offset:1024 nt
	global_load_lds_dwordx4 v34, s[16:17] offset:2048 nt
	global_load_lds_dwordx4 v35, s[16:17] offset:3072 nt
	s_add_u32 s16, s16, 0x7d00
	s_addc_u32 s17, s17, 0
	v_cndmask_b32_e64 v30, 0, v30, s[18:19]
	v_cndmask_b32_e64 v31, 0, v31, s[18:19]
	v_cndmask_b32_e64 v32, 0, v32, s[18:19]
	v_cndmask_b32_e64 v33, 0, v33, s[18:19]
	v_max3_f32 v41, |v18|, |v19|, |v20|
	v_max3_f32 v42, |v21|, |v22|, |v23|
	v_max3_f32 v43, |v24|, |v25|, |v26|
	v_max3_f32 v44, |v27|, |v28|, |v29|
	v_max3_f32 v48, |v30|, |v31|, |v32|
	v_max3_f32 v41, v41, v42, |v33|
	v_max3_f32 v43, v43, v44, v48
	v_max_f32_e32 v41, v41, v43
	v_pk_add_f32 v[2:3], v[2:3], v[18:19]
	v_pk_add_f32 v[4:5], v[4:5], v[20:21]
	v_max_f32_dpp v41, v41, v41 quad_perm:[1,0,3,2] row_mask:0xf bank_mask:0xf
	v_pk_add_f32 v[6:7], v[6:7], v[22:23]
	v_pk_add_f32 v[8:9], v[8:9], v[24:25]
	v_max_f32_dpp v41, v41, v41 quad_perm:[2,3,0,1] row_mask:0xf bank_mask:0xf
	v_pk_add_f32 v[10:11], v[10:11], v[26:27]
	v_pk_add_f32 v[12:13], v[12:13], v[28:29]
	v_max_f32_dpp v41, v41, v41 row_half_mirror row_mask:0xf bank_mask:0xf
	v_pk_add_f32 v[14:15], v[14:15], v[30:31]
	v_pk_add_f32 v[16:17], v[16:17], v[32:33]
	v_max_f32_dpp v41, v41, v41 row_mirror row_mask:0xf bank_mask:0xf
	s_nop 1
	v_max_f32_dpp v41, v41, v41 row_bcast:15 row_mask:0xa bank_mask:0xf
	s_nop 1
	v_max_f32_dpp v41, v41, v41 row_bcast:31 row_mask:0xc bank_mask:0xf
	s_nop 1
	v_readlane_b32 s28, v41, 63
	s_nop 1
	v_div_scale_f32 v48, s[30:31], s28, s28, v47
	v_rcp_f32_e32 v49, v48
	s_nop 0
	v_fma_f32 v50, -v48, v49, 1.0
	v_fmac_f32_e32 v49, v50, v49
	v_mov_b32_e32 v50, s28
	v_div_scale_f32 v50, vcc, s32, v50, s32
	v_mul_f32_e32 v51, v50, v49
	v_fma_f32 v52, -v48, v51, v50
	v_fmac_f32_e32 v51, v52, v49
	v_fma_f32 v48, -v48, v51, v50
	v_div_fmas_f32 v48, v48, v49, v51
	v_div_fixup_f32 v48, v48, s28, v47
	v_cmp_gt_f32_e64 vcc, s28, 0
	v_writelane_b32 v40, s28, 22
	s_nop 0
	v_cndmask_b32_e32 v48, 0, v48, vcc
	v_fmaak_f32 v49, v18, v48, 0x4b400000
	v_fmaak_f32 v50, v19, v48, 0x4b400000
	v_fmaak_f32 v51, v20, v48, 0x4b400000
	v_fmaak_f32 v52, v21, v48, 0x4b400000
	v_perm_b32 v49, v50, v49, s33
	v_perm_b32 v51, v52, v51, s34
	v_or_b32_e32 v49, v49, v51
	s_add_u32 s20, s20, 0x400
	s_addc_u32 s21, s21, 0
	s_add_u32 s22, s22, 0x400
	s_addc_u32 s23, s23, 0
	s_add_u32 s24, s24, 0x400
	s_addc_u32 s25, s25, 0
	s_add_u32 s26, s26, 0x400
	s_addc_u32 s27, s27, 0
	global_store_dword v39, v49, s[20:21]
	v_fmaak_f32 v41, v22, v48, 0x4b400000
	v_fmaak_f32 v42, v23, v48, 0x4b400000
	v_fmaak_f32 v43, v24, v48, 0x4b400000
	v_fmaak_f32 v44, v25, v48, 0x4b400000
	v_perm_b32 v41, v42, v41, s33
	v_perm_b32 v43, v44, v43, s34
	v_or_b32_e32 v41, v41, v43
	global_store_dword v39, v41, s[22:23]
	v_fmaak_f32 v49, v26, v48, 0x4b400000
	v_fmaak_f32 v50, v27, v48, 0x4b400000
	v_fmaak_f32 v51, v28, v48, 0x4b400000
	v_fmaak_f32 v52, v29, v48, 0x4b400000
	v_perm_b32 v49, v50, v49, s33
	v_perm_b32 v51, v52, v51, s34
	v_or_b32_e32 v49, v49, v51
	global_store_dword v39, v49, s[24:25]
	v_fmaak_f32 v41, v30, v48, 0x4b400000
	v_fmaak_f32 v42, v31, v48, 0x4b400000
	v_fmaak_f32 v43, v32, v48, 0x4b400000
	v_fmaak_f32 v44, v33, v48, 0x4b400000
	v_perm_b32 v41, v42, v41, s33
	v_perm_b32 v43, v44, v43, s34
	v_or_b32_e32 v41, v41, v43
	global_store_dword v39, v41, s[26:27]
	s_waitcnt vmcnt(4)
	ds_read_b128 v[18:21], v38 offset:4096
	ds_read_b128 v[22:25], v38 offset:5120
	ds_read_b128 v[26:29], v38 offset:6144
	ds_read_b128 v[30:33], v38 offset:7168
	s_waitcnt lgkmcnt(0)
	s_cmp_eq_u32 s29, 1
	s_cbranch_scc0 .Lk1_nodma24
	s_mov_b32 m0, s35
	s_nop 0
	global_load_lds_dwordx4 v34, s[16:17] nt
	global_load_lds_dwordx4 v34, s[16:17] offset:1024 nt
	global_load_lds_dwordx4 v34, s[16:17] offset:2048 nt
	global_load_lds_dwordx4 v35, s[16:17] offset:3072 nt
	s_add_u32 s16, s16, 0x7d00
	s_addc_u32 s17, s17, 0
